# in-proj 128x128 tile epilogues (two instances): 8 serialized (scale load, full wait) pairs per tile replaced by 8 loads issued together with one wait; later load sites are register copies
# speedup vs baseline: 1.0096x; 1.0038x over previous
; template <bool I8 = false>
; __device__ __forceinline__ void gemm_mainloop(const bf16_t* __restrict__ A, int lda, const bf16_t* __restrict__ Bt, int ldb,
;                                               int K, int m0, int n0, f32x4 (&acc)[4][4], char* smem) {
;     ...
;   for (int kt = 0; kt < nk; ++kt) {
;     const int cur = kt & 1;
;     if (kt + 1 < nk) GSTAGE(cur ^ 1, kt + 1);
;     const char* sA = smem + cur * 32768;
;     const char* sB = sA + 16384;
; #pragma unroll
;     for (int kk = 0; kk < 2; ++kk) {
;       bf16x8 af[4], bfr[4];
;       const int ch = kk * 4 + (lane >> 4);
; #pragma unroll
;       for (int i = 0; i < 4; ++i) {
;         int row = wm * 64 + i * 16 + (lane & 15);
;         af[i] = *reinterpret_cast<const bf16x8*>(sA + row * 128 + ((ch ^ (row & 7)) << 4));
;         int col = wn * 64 + i * 16 + (lane & 15);
;         bfr[i] = *reinterpret_cast<const bf16x8*>(sB + col * 128 + ((ch ^ (col & 7)) << 4));
;       }
; #pragma unroll
;       for (int i = 0; i < 4; ++i)
; #pragma unroll
;         for (int j = 0; j < 4; ++j) {
;           if (I8) {
;             typedef __attribute__((ext_vector_type(4))) int i32x4;
;             acc[i][j] = __builtin_bit_cast(f32x4, __builtin_amdgcn_mfma_i32_16x16x64_i8(__builtin_bit_cast(i32x4, af[i]), __builtin_bit_cast(i32x4, bfr[j]),
;                                                                                          __builtin_bit_cast(i32x4, acc[i][j]), 0, 0, 0));
;           } else {
;             acc[i][j] = __builtin_amdgcn_mfma_f32_16x16x32_bf16(af[i], bfr[j], acc[i][j], 0, 0, 0);
;           }
;         }
;     }
;     asm volatile("s_waitcnt vmcnt(0)" ::: "memory");
;     __syncthreads();
;   }
.LBB0_237:
	v_lshl_add_u64 v[76:77], v[68:69], 0, s[6:7]
	s_mov_b64 s[10:11], 0x1000080
	s_and_b32 s12, s9, 0x8000
	v_lshl_add_u64 v[80:81], v[76:77], 0, s[10:11]
	s_mov_b64 s[10:11], 0x1010080
	s_xor_b32 s13, s12, 0x8000
	v_lshl_add_u64 v[84:85], v[76:77], 0, s[10:11]
	s_mov_b64 s[10:11], 0x1020080
	v_lshl_add_u64 v[88:89], v[76:77], 0, s[10:11]
	s_mov_b64 s[10:11], 0x1030080
	v_add_u32_e32 v92, s13, v73
	v_lshl_add_u64 v[76:77], v[76:77], 0, s[10:11]
	v_readfirstlane_b32 s10, v92
	v_add_u32_e32 v93, 0x4000, v92
	v_lshl_add_u64 v[78:79], v[66:67], 0, s[6:7]
	v_add_u32_e32 v94, 0x1000, v92
	v_readfirstlane_b32 s11, v93
	s_mov_b32 m0, s10
	v_lshl_add_u64 v[82:83], v[78:79], 0, s[60:61]
	v_add_u32_e32 v95, 0x5000, v92
	v_readfirstlane_b32 s13, v94
	global_load_lds_dwordx4 v[80:81], off
	s_mov_b32 m0, s11
	v_add_u32_e32 v97, 0x2000, v92
	v_readfirstlane_b32 s14, v95
	global_load_lds_dwordx4 v[82:83], off
	s_mov_b32 m0, s13
	v_lshl_add_u64 v[86:87], v[78:79], 0, s[62:63]
	v_add_u32_e32 v98, 0x6000, v92
	v_readfirstlane_b32 s15, v97
	global_load_lds_dwordx4 v[84:85], off
	s_mov_b32 m0, s14
	v_add_u32_e32 v99, 0x3000, v92
	v_readfirstlane_b32 s16, v98
	global_load_lds_dwordx4 v[86:87], off
	s_mov_b32 m0, s15
	v_lshl_add_u64 v[90:91], v[78:79], 0, s[64:65]
	v_add_u32_e32 v92, 0x7000, v92
	v_readfirstlane_b32 s17, v99
	global_load_lds_dwordx4 v[88:89], off
	s_mov_b32 m0, s16
	v_readfirstlane_b32 s76, v92
	global_load_lds_dwordx4 v[90:91], off
	s_mov_b32 m0, s17
	v_lshl_add_u64 v[78:79], v[78:79], 0, s[66:67]
	global_load_lds_dwordx4 v[76:77], off
	s_mov_b32 m0, s76
	v_or_b32_e32 v75, s12, v74
	global_load_lds_dwordx4 v[78:79], off
	v_add_u32_e32 v96, v75, v71
	v_add_u32_e32 v75, v75, v70
	ds_read_b128 v[76:79], v96
	ds_read_b128 v[80:83], v75 offset:16384
	ds_read_b128 v[84:87], v75 offset:18432
	ds_read_b128 v[88:91], v75 offset:20480
	ds_read_b128 v[92:95], v75 offset:22528
	s_waitcnt lgkmcnt(0)
	v_mfma_i32_16x16x64_i8 v[62:65], v[76:79], v[80:83], v[62:65]
	v_or_b32_e32 v75, s12, v72
	s_add_i32 s9, s9, 0x8000
	s_add_u32 s6, s6, 0x80
	v_mfma_i32_16x16x64_i8 v[58:61], v[76:79], v[84:87], v[58:61]
	s_addc_u32 s7, s7, 0
	s_cmpk_lg_i32 s6, 0x780
	v_mfma_i32_16x16x64_i8 v[54:57], v[76:79], v[88:91], v[54:57]
	v_mfma_i32_16x16x64_i8 v[50:53], v[76:79], v[92:95], v[50:53]
	ds_read_b128 v[76:79], v96 offset:2048
	s_waitcnt lgkmcnt(0)
	v_mfma_i32_16x16x64_i8 v[46:49], v[76:79], v[80:83], v[46:49]
	v_mfma_i32_16x16x64_i8 v[38:41], v[76:79], v[84:87], v[38:41]
	v_mfma_i32_16x16x64_i8 v[34:37], v[76:79], v[88:91], v[34:37]
	v_mfma_i32_16x16x64_i8 v[26:29], v[76:79], v[92:95], v[26:29]
	ds_read_b128 v[76:79], v96 offset:4096
	s_waitcnt lgkmcnt(0)
	v_mfma_i32_16x16x64_i8 v[22:25], v[76:79], v[80:83], v[22:25]
	v_mfma_i32_16x16x64_i8 v[18:21], v[76:79], v[84:87], v[18:21]
	v_mfma_i32_16x16x64_i8 v[14:17], v[76:79], v[88:91], v[14:17]
	v_mfma_i32_16x16x64_i8 v[10:13], v[76:79], v[92:95], v[10:13]
	ds_read_b128 v[76:79], v96 offset:6144
	v_add_u32_e32 v96, v75, v71
	v_add_u32_e32 v75, v75, v70
	s_waitcnt lgkmcnt(0)
	v_mfma_i32_16x16x64_i8 v[6:9], v[76:79], v[80:83], v[6:9]
	ds_read_b128 v[80:83], v96
	v_mfma_i32_16x16x64_i8 v[2:5], v[76:79], v[84:87], v[2:5]
	ds_read_b128 v[84:87], v75 offset:18432
	v_mfma_i32_16x16x64_i8 v[42:45], v[76:79], v[88:91], v[42:45]
	ds_read_b128 v[88:91], v75 offset:20480
	v_mfma_i32_16x16x64_i8 v[30:33], v[76:79], v[92:95], v[30:33]
	ds_read_b128 v[76:79], v75 offset:16384
	ds_read_b128 v[92:95], v75 offset:22528
	s_waitcnt lgkmcnt(0)
	v_mfma_i32_16x16x64_i8 v[62:65], v[80:83], v[76:79], v[62:65]
	v_mfma_i32_16x16x64_i8 v[58:61], v[80:83], v[84:87], v[58:61]
	v_mfma_i32_16x16x64_i8 v[54:57], v[80:83], v[88:91], v[54:57]
	v_mfma_i32_16x16x64_i8 v[50:53], v[80:83], v[92:95], v[50:53]
	ds_read_b128 v[80:83], v96 offset:2048
	s_waitcnt lgkmcnt(0)
	v_mfma_i32_16x16x64_i8 v[46:49], v[80:83], v[76:79], v[46:49]
	v_mfma_i32_16x16x64_i8 v[38:41], v[80:83], v[84:87], v[38:41]
	v_mfma_i32_16x16x64_i8 v[34:37], v[80:83], v[88:91], v[34:37]
	v_mfma_i32_16x16x64_i8 v[26:29], v[80:83], v[92:95], v[26:29]
	ds_read_b128 v[80:83], v96 offset:4096
	s_waitcnt lgkmcnt(0)
	v_mfma_i32_16x16x64_i8 v[22:25], v[80:83], v[76:79], v[22:25]
	v_mfma_i32_16x16x64_i8 v[18:21], v[80:83], v[84:87], v[18:21]
	v_mfma_i32_16x16x64_i8 v[14:17], v[80:83], v[88:91], v[14:17]
	v_mfma_i32_16x16x64_i8 v[10:13], v[80:83], v[92:95], v[10:13]
	ds_read_b128 v[80:83], v96 offset:6144
	s_waitcnt vmcnt(0)
	s_waitcnt vmcnt(0) lgkmcnt(0)
	v_mfma_i32_16x16x64_i8 v[6:9], v[80:83], v[76:79], v[6:9]
	s_barrier
	v_mfma_i32_16x16x64_i8 v[2:5], v[80:83], v[84:87], v[2:5]
	v_mfma_i32_16x16x64_i8 v[42:45], v[80:83], v[88:91], v[42:45]
	v_mfma_i32_16x16x64_i8 v[30:33], v[80:83], v[92:95], v[30:33]
	s_cbranch_scc1 .LBB0_237
; template <bool I8 = false, class Epi> ...
;     ...
;   gemm_mainloop<I8>(A, lda, Bt, ldb, K, m0, n0, acc, smem);
; #pragma unroll
;   for (int i = 0; i < 4; ++i) {
;     const int row = m0 + wm * 64 + i * 16 + (lane >> 4) * 4;
;     float4 rs = float4{1.f, 1.f, 1.f, 1.f};
;     if (I8) rs = *reinterpret_cast<const float4*>(rscale + row);
; #pragma unroll
;     for (int j = 0; j < 4; ++j) {
;       const int col = n0 + wn * 64 + j * 16 + (lane & 15);
;       if (I8) {
;         typedef __attribute__((ext_vector_type(4))) int i32x4;
;         const i32x4 ia = __builtin_bit_cast(i32x4, acc[i][j]);
;         const float cs = cscale[col];
;         epi(row, col, f32x4{(float)ia[0] * rs.x * cs, (float)ia[1] * rs.y * cs, (float)ia[2] * rs.z * cs, (float)ia[3] * rs.w * cs});
;       } else {
;         epi(row, col, acc[i][j]);
;       }
;     }
;   __device__ __forceinline__ void operator()(int row, int col, f32x4 v) const {
;     if (col < 2048) {
;       int ch = col & 1023, half = col >> 10;
;       int b = row / seqlen, l = row - b * seqlen;
;       uint2 pk; pk.x = pack2(v[0], v[1]); pk.y = pack2(v[2], v[3]);
;       *reinterpret_cast<uint2*>(ABt + ((size_t)(b * 1024 + ch) * 4096 + half * 2048 + l)) = pk;
;     } else if (col < 3072) {
; #pragma unroll
;       for (int r = 0; r < 4; ++r) z[(size_t)(row + r) * 1024 + (col - 2048)] = f2bf(v[r]);
;     } else if (col < 4608) {
; #pragma unroll
;       for (int r = 0; r < 4; ++r) xbcraw[(size_t)(row + r) * DXBC + (col - 3072)] = f2bf(v[r]);
;     } else if (col < 4640) {
; #pragma unroll
;       for (int r = 0; r < 4; ++r) dtraw[(size_t)(row + r) * 32 + (col - 4608)] = v[r];
;     }
;   }
	v_add_u32_e32 v73, v74, v71
	ds_read_b128 v[66:69], v73 offset:32768
	v_add_u32_e32 v86, v74, v70
	ds_read_b128 v[74:77], v86 offset:49152
	ds_read_b128 v[78:81], v86 offset:51200
	ds_read_b128 v[82:85], v86 offset:53248
	ds_read_b128 v[86:89], v86 offset:55296
	v_add_u32_e32 v71, v72, v71
	v_or_b32_e32 v136, s91, v164
	v_lshl_add_u64 v[106:107], v[136:137], 2, s[26:27]
	s_waitcnt lgkmcnt(0)
	v_mfma_i32_16x16x64_i8 v[90:93], v[66:69], v[86:89], v[50:53]
	s_cmpk_gt_u32 s91, 0x7ff
	s_cselect_b64 s[14:15], -1, 0
	s_nop 0
	ds_read_b128 v[50:53], v73 offset:34816
	v_mfma_i32_16x16x64_i8 v[58:61], v[66:69], v[78:81], v[58:61]
	s_and_b64 vcc, exec, s[14:15]
	s_waitcnt lgkmcnt(0)
	v_mfma_i32_16x16x64_i8 v[46:49], v[50:53], v[74:77], v[46:49]
	v_mfma_i32_16x16x64_i8 v[38:41], v[50:53], v[78:81], v[38:41]
	v_mfma_i32_16x16x64_i8 v[34:37], v[50:53], v[82:85], v[34:37]
	v_mfma_i32_16x16x64_i8 v[26:29], v[50:53], v[86:89], v[26:29]
	ds_read_b128 v[50:53], v73 offset:36864
	s_waitcnt lgkmcnt(0)
	v_mfma_i32_16x16x64_i8 v[22:25], v[50:53], v[74:77], v[22:25]
	v_mfma_i32_16x16x64_i8 v[18:21], v[50:53], v[78:81], v[18:21]
	v_mfma_i32_16x16x64_i8 v[14:17], v[50:53], v[82:85], v[14:17]
	v_mfma_i32_16x16x64_i8 v[108:111], v[50:53], v[86:89], v[10:13]
	ds_read_b128 v[50:53], v73 offset:38912
	s_waitcnt lgkmcnt(0)
	v_mfma_i32_16x16x64_i8 v[2:5], v[50:53], v[78:81], v[2:5]
	v_add_u32_e32 v78, s8, v145
	v_ashrrev_i32_e32 v79, 31, v78
	v_or_b32_e32 v98, 1, v78
	v_mfma_i32_16x16x64_i8 v[62:65], v[66:69], v[74:77], v[62:65]
	v_or_b32_e32 v100, 2, v78
	v_or_b32_e32 v132, 3, v78
	v_ashrrev_i32_e32 v99, 31, v98
	v_mfma_i32_16x16x64_i8 v[54:57], v[66:69], v[82:85], v[54:57]
	v_ashrrev_i32_e32 v101, 31, v100
	v_ashrrev_i32_e32 v133, 31, v132
	v_mad_i64_i32 v[96:97], s[6:7], v78, s83, 0
	v_mfma_i32_16x16x64_i8 v[10:13], v[50:53], v[74:77], v[6:9]
	v_add_u32_e32 v74, v72, v70
	v_lshlrev_b64 v[94:95], 7, v[78:79]
	v_lshlrev_b64 v[104:105], 11, v[78:79]
	v_mfma_i32_16x16x64_i8 v[66:69], v[50:53], v[86:89], v[30:33]
	v_mad_i64_i32 v[86:87], s[6:7], v100, s83, 0
	v_lshlrev_b64 v[88:89], 7, v[100:101]
	s_nop 0
	v_lshl_add_u64 v[30:31], v[78:79], 2, s[52:53]
	v_mfma_i32_16x16x64_i8 v[6:9], v[50:53], v[82:85], v[42:45]
	s_nop 2
	ds_read_b128 v[42:45], v71 offset:32768
	ds_read_b128 v[82:85], v71 offset:34816
	ds_read_b128 v[112:115], v74 offset:49152
	ds_read_b128 v[116:119], v74 offset:51200
	ds_read_b128 v[120:123], v71 offset:36864
	ds_read_b128 v[70:73], v71 offset:38912
	ds_read_b128 v[124:127], v74 offset:53248
	ds_read_b128 v[74:77], v74 offset:55296
	s_waitcnt vmcnt(0)
	s_waitcnt lgkmcnt(0)
	s_barrier
	global_load_dwordx4 v[50:53], v[30:31], off
	global_load_dword v80, v[106:107], off
	global_load_dwordx4 v[212:215], v[30:31], off offset:64
	global_load_dwordx4 v[216:219], v[30:31], off offset:128
	global_load_dwordx4 v[220:223], v[30:31], off offset:192
	global_load_dword v225, v[106:107], off offset:64
	global_load_dword v226, v[106:107], off offset:128
	global_load_dword v227, v[106:107], off offset:192
	v_mfma_i32_16x16x64_i8 v[128:131], v[42:45], v[112:115], v[62:65]
	v_lshlrev_b64 v[102:103], 11, v[98:99]
	v_lshlrev_b64 v[100:101], 11, v[100:101]
	v_mfma_i32_16x16x64_i8 v[62:65], v[42:45], v[116:119], v[58:61]
	v_mfma_i32_16x16x64_i8 v[58:61], v[42:45], v[124:127], v[54:57]
	v_mfma_i32_16x16x64_i8 v[54:57], v[42:45], v[74:77], v[90:93]
	v_mfma_i32_16x16x64_i8 v[42:45], v[82:85], v[116:119], v[38:41]
	s_nop 1
	v_mad_i64_i32 v[90:91], s[6:7], v98, s83, 0
	v_lshlrev_b64 v[92:93], 7, v[98:99]
	v_mfma_i32_16x16x64_i8 v[38:41], v[82:85], v[124:127], v[34:37]
	v_lshlrev_b64 v[98:99], 11, v[132:133]
	v_mfma_i32_16x16x64_i8 v[34:37], v[82:85], v[74:77], v[26:29]
	v_mfma_i32_16x16x64_i8 v[26:29], v[120:123], v[116:119], v[18:21]
	v_mfma_i32_16x16x64_i8 v[18:21], v[120:123], v[74:77], v[108:111]
	s_nop 2
	v_cvt_f32_i32_e32 v109, v129
	v_cvt_f32_i32_e32 v108, v128
	v_cvt_f32_i32_e32 v111, v131
	v_cvt_f32_i32_e32 v110, v130
	v_mfma_i32_16x16x64_i8 v[30:33], v[120:123], v[112:115], v[22:25]
	v_mfma_i32_16x16x64_i8 v[22:25], v[120:123], v[124:127], v[14:17]
	v_mfma_i32_16x16x64_i8 v[14:17], v[70:73], v[112:115], v[10:13]
	v_mfma_i32_16x16x64_i8 v[46:49], v[82:85], v[112:115], v[46:49]
	v_mad_i64_i32 v[82:83], s[6:7], v132, s83, 0
	v_lshlrev_b64 v[84:85], 7, v[132:133]
	v_mfma_i32_16x16x64_i8 v[6:9], v[70:73], v[124:127], v[6:9]
	s_mov_b64 s[6:7], -1
	s_waitcnt vmcnt(0)
	v_pk_mul_f32 v[10:11], v[50:51], v[108:109]
	s_waitcnt vmcnt(0)
	v_pk_mul_f32 v[108:109], v[10:11], v[80:81] op_sel_hi:[1,0]
	v_mfma_i32_16x16x64_i8 v[10:13], v[70:73], v[116:119], v[2:5]
	s_nop 2
	v_mul_f32_e64 v2, v52, v110
	v_mul_f32_e64 v3, v53, v111
	v_pk_mul_f32 v[110:111], v[2:3], v[80:81] op_sel_hi:[1,0]
	v_mfma_i32_16x16x64_i8 v[2:5], v[70:73], v[74:77], v[66:69]
	s_cbranch_vccz .LBB0_250
	s_cmp_lt_u32 s94, 0xfffff400
	s_cbranch_scc0 .LBB0_247
	s_cmpk_gt_u32 s91, 0x11ff
	s_cbranch_scc0 .LBB0_244
	v_cmp_gt_u32_e32 vcc, s85, v136
	s_and_saveexec_b64 s[6:7], vcc
	s_cbranch_execz .LBB0_243
	v_lshl_add_u64 v[66:67], v[136:137], 2, s[30:31]
	v_lshl_add_u64 v[68:69], v[66:67], 0, v[94:95]
	v_add_co_u32_e32 v68, vcc, 0xffffc000, v68
	s_nop 1
	v_addc_co_u32_e32 v69, vcc, -1, v69, vcc
	global_store_dword v[68:69], v108, off offset:-2048
	v_lshl_add_u64 v[68:69], v[66:67], 0, v[92:93]
	v_add_co_u32_e32 v68, vcc, 0xffffc000, v68
	s_nop 1
	v_addc_co_u32_e32 v69, vcc, -1, v69, vcc
	global_store_dword v[68:69], v109, off offset:-2048
	v_lshl_add_u64 v[68:69], v[66:67], 0, v[88:89]
	v_add_co_u32_e32 v68, vcc, 0xffffc000, v68
	v_lshl_add_u64 v[66:67], v[66:67], 0, v[84:85]
	s_nop 0
	v_addc_co_u32_e32 v69, vcc, -1, v69, vcc
	v_add_co_u32_e32 v66, vcc, 0xffffc000, v66
	global_store_dword v[68:69], v110, off offset:-2048
	s_nop 0
	v_addc_co_u32_e32 v67, vcc, -1, v67, vcc
	global_store_dword v[66:67], v111, off offset:-2048

; template <bool I8 = false, class Epi> ...
;     ...
;       const int col = n0 + wn * 64 + j * 16 + (lane & 15);
;       if (I8) {
;         typedef __attribute__((ext_vector_type(4))) int i32x4;
;         const i32x4 ia = __builtin_bit_cast(i32x4, acc[i][j]);
;         const float cs = cscale[col];
;         epi(row, col, f32x4{(float)ia[0] * rs.x * cs, (float)ia[1] * rs.y * cs, (float)ia[2] * rs.z * cs, (float)ia[3] * rs.w * cs});
;       } else {
;         epi(row, col, acc[i][j]);
;       }
;     }
;   __device__ __forceinline__ void operator()(int row, int col, f32x4 v) const {
;     if (col < 2048) {
;       int ch = col & 1023, half = col >> 10;
;       int b = row / seqlen, l = row - b * seqlen;
;       uint2 pk; pk.x = pack2(v[0], v[1]); pk.y = pack2(v[2], v[3]);
;       *reinterpret_cast<uint2*>(ABt + ((size_t)(b * 1024 + ch) * 4096 + half * 2048 + l)) = pk;
;     } else if (col < 3072) {
; #pragma unroll
;       for (int r = 0; r < 4; ++r) z[(size_t)(row + r) * 1024 + (col - 2048)] = f2bf(v[r]);
;     } else if (col < 4608) {
; #pragma unroll
;       for (int r = 0; r < 4; ++r) xbcraw[(size_t)(row + r) * DXBC + (col - 3072)] = f2bf(v[r]);
;     } else if (col < 4640) {
; #pragma unroll
;       for (int r = 0; r < 4; ++r) dtraw[(size_t)(row + r) * 32 + (col - 4608)] = v[r];
;     }
;   }
.LBB0_252:
	v_mov_b32_e32 v66, v225
	v_cvt_f32_i32_e32 v63, v63
	v_cvt_f32_i32_e32 v62, v62
	v_cvt_f32_i32_e32 v65, v65
	v_cvt_f32_i32_e32 v64, v64
	s_movk_i32 s6, 0x7ef
	v_pk_mul_f32 v[62:63], v[50:51], v[62:63]
	v_cmp_lt_u32_e64 s[6:7], s6, v136
	v_pk_mul_f32 v[68:69], v[52:53], v[64:65]
	v_pk_mul_f32 v[64:65], v[62:63], v[66:67] op_sel_hi:[1,0]
	v_pk_mul_f32 v[62:63], v[68:69], v[66:67] op_sel_hi:[1,0]
	s_and_saveexec_b64 s[8:9], s[6:7]
	s_xor_b64 s[8:9], exec, s[8:9]
	s_cbranch_execz .LBB0_264
	v_cmp_lt_u32_e32 vcc, s88, v136
	s_and_saveexec_b64 s[10:11], vcc
	s_xor_b64 s[10:11], exec, s[10:11]
	s_cbranch_execz .LBB0_261
	v_cmp_lt_u32_e32 vcc, s89, v136
	s_and_saveexec_b64 s[12:13], vcc
	s_xor_b64 s[12:13], exec, s[12:13]
	s_cbranch_execz .LBB0_258
	v_cmp_gt_u32_e32 vcc, s90, v136
	s_and_saveexec_b64 s[16:17], vcc
	s_cbranch_execz .LBB0_257
	v_lshl_add_u64 v[68:69], v[136:137], 2, s[30:31]
	v_lshl_add_u64 v[70:71], v[68:69], 0, v[94:95]
	v_add_co_u32_e32 v70, vcc, 0xffffc000, v70
	s_nop 1
	v_addc_co_u32_e32 v71, vcc, -1, v71, vcc
	global_store_dword v[70:71], v64, off offset:-1984
	v_lshl_add_u64 v[70:71], v[68:69], 0, v[92:93]
	v_add_co_u32_e32 v70, vcc, 0xffffc000, v70
	s_nop 1
	v_addc_co_u32_e32 v71, vcc, -1, v71, vcc
	global_store_dword v[70:71], v65, off offset:-1984
	v_lshl_add_u64 v[64:65], v[68:69], 0, v[88:89]
	v_add_co_u32_e32 v64, vcc, 0xffffc000, v64
	s_nop 1
	v_addc_co_u32_e32 v65, vcc, -1, v65, vcc
	global_store_dword v[64:65], v62, off offset:-1984
	v_lshl_add_u64 v[64:65], v[68:69], 0, v[84:85]
	v_add_co_u32_e32 v64, vcc, 0xffffc000, v64
	s_nop 1
	v_addc_co_u32_e32 v65, vcc, -1, v65, vcc
	global_store_dword v[64:65], v63, off offset:-1984

; template <bool I8 = false, class Epi> ...
;     ...
;       const int col = n0 + wn * 64 + j * 16 + (lane & 15);
;       if (I8) {
;         typedef __attribute__((ext_vector_type(4))) int i32x4;
;         const i32x4 ia = __builtin_bit_cast(i32x4, acc[i][j]);
;         const float cs = cscale[col];
;         epi(row, col, f32x4{(float)ia[0] * rs.x * cs, (float)ia[1] * rs.y * cs, (float)ia[2] * rs.z * cs, (float)ia[3] * rs.w * cs});
;       } else {
;         epi(row, col, acc[i][j]);
;       }
;     }
;   __device__ __forceinline__ void operator()(int row, int col, f32x4 v) const {
;     if (col < 2048) {
;       int ch = col & 1023, half = col >> 10;
;       int b = row / seqlen, l = row - b * seqlen;
;       uint2 pk; pk.x = pack2(v[0], v[1]); pk.y = pack2(v[2], v[3]);
;       *reinterpret_cast<uint2*>(ABt + ((size_t)(b * 1024 + ch) * 4096 + half * 2048 + l)) = pk;
;     } else if (col < 3072) {
; #pragma unroll
;       for (int r = 0; r < 4; ++r) z[(size_t)(row + r) * 1024 + (col - 2048)] = f2bf(v[r]);
;     } else if (col < 4608) {
; #pragma unroll
;       for (int r = 0; r < 4; ++r) xbcraw[(size_t)(row + r) * DXBC + (col - 3072)] = f2bf(v[r]);
;     } else if (col < 4640) {
; #pragma unroll
;       for (int r = 0; r < 4; ++r) dtraw[(size_t)(row + r) * 32 + (col - 4608)] = v[r];
;     }
;   }
.LBB0_266:
	s_or_b64 exec, exec, s[8:9]
	v_mov_b32_e32 v62, v226
	v_cvt_f32_i32_e32 v59, v59
	v_cvt_f32_i32_e32 v58, v58
	v_cvt_f32_i32_e32 v61, v61
	v_cvt_f32_i32_e32 v60, v60
	s_movk_i32 s8, 0x7df
	v_pk_mul_f32 v[58:59], v[50:51], v[58:59]
	v_cmp_lt_u32_e64 s[8:9], s8, v136
	v_pk_mul_f32 v[64:65], v[52:53], v[60:61]
	v_pk_mul_f32 v[60:61], v[58:59], v[62:63] op_sel_hi:[1,0]
	v_pk_mul_f32 v[58:59], v[64:65], v[62:63] op_sel_hi:[1,0]
	s_and_saveexec_b64 s[10:11], s[8:9]
	s_xor_b64 s[10:11], exec, s[10:11]
	s_cbranch_execz .LBB0_277
	v_cmp_lt_u32_e32 vcc, s92, v136
	s_and_saveexec_b64 s[12:13], vcc
	s_xor_b64 s[12:13], exec, s[12:13]
	s_cbranch_execz .LBB0_274
	v_cmp_lt_u32_e32 vcc, s93, v136
	s_and_saveexec_b64 s[16:17], vcc
	s_xor_b64 s[16:17], exec, s[16:17]
	s_cbranch_execz .LBB0_271
	s_cmpk_gt_u32 s91, 0x11ff
	s_cbranch_scc1 .LBB0_271
	v_lshl_add_u64 v[64:65], v[136:137], 2, s[30:31]
	v_lshl_add_u64 v[68:69], v[64:65], 0, v[94:95]
	v_add_co_u32_e32 v68, vcc, 0xffffc000, v68
	s_nop 1
	v_addc_co_u32_e32 v69, vcc, -1, v69, vcc
	global_store_dword v[68:69], v60, off offset:-1920
	v_lshl_add_u64 v[68:69], v[64:65], 0, v[92:93]
	v_add_co_u32_e32 v68, vcc, 0xffffc000, v68
	s_nop 1
	v_addc_co_u32_e32 v69, vcc, -1, v69, vcc
	global_store_dword v[68:69], v61, off offset:-1920
	v_lshl_add_u64 v[60:61], v[64:65], 0, v[88:89]
	v_add_co_u32_e32 v60, vcc, 0xffffc000, v60
	s_nop 1
	v_addc_co_u32_e32 v61, vcc, -1, v61, vcc
	global_store_dword v[60:61], v58, off offset:-1920
	v_lshl_add_u64 v[60:61], v[64:65], 0, v[84:85]
	v_add_co_u32_e32 v60, vcc, 0xffffc000, v60
	s_nop 1
	v_addc_co_u32_e32 v61, vcc, -1, v61, vcc
	global_store_dword v[60:61], v59, off offset:-1920

; template <bool I8 = false, class Epi> ...
;     ...
;       const int col = n0 + wn * 64 + j * 16 + (lane & 15);
;       if (I8) {
;         typedef __attribute__((ext_vector_type(4))) int i32x4;
;         const i32x4 ia = __builtin_bit_cast(i32x4, acc[i][j]);
;         const float cs = cscale[col];
;         epi(row, col, f32x4{(float)ia[0] * rs.x * cs, (float)ia[1] * rs.y * cs, (float)ia[2] * rs.z * cs, (float)ia[3] * rs.w * cs});
;       } else {
;         epi(row, col, acc[i][j]);
;       }
;     }
;   __device__ __forceinline__ void operator()(int row, int col, f32x4 v) const {
;     if (col < 2048) {
;       int ch = col & 1023, half = col >> 10;
;       int b = row / seqlen, l = row - b * seqlen;
;       uint2 pk; pk.x = pack2(v[0], v[1]); pk.y = pack2(v[2], v[3]);
;       *reinterpret_cast<uint2*>(ABt + ((size_t)(b * 1024 + ch) * 4096 + half * 2048 + l)) = pk;
;     } else if (col < 3072) {
; #pragma unroll
;       for (int r = 0; r < 4; ++r) z[(size_t)(row + r) * 1024 + (col - 2048)] = f2bf(v[r]);
;     } else if (col < 4608) {
; #pragma unroll
;       for (int r = 0; r < 4; ++r) xbcraw[(size_t)(row + r) * DXBC + (col - 3072)] = f2bf(v[r]);
;     } else if (col < 4640) {
; #pragma unroll
;       for (int r = 0; r < 4; ++r) dtraw[(size_t)(row + r) * 32 + (col - 4608)] = v[r];
;     }
;   }
.LBB0_279:
	s_or_b64 exec, exec, s[10:11]
	v_mov_b32_e32 v58, v227
	v_cvt_f32_i32_e32 v55, v55
	v_cvt_f32_i32_e32 v54, v54
	v_cvt_f32_i32_e32 v57, v57
	v_cvt_f32_i32_e32 v56, v56
	s_movk_i32 s10, 0x7cf
	v_pk_mul_f32 v[50:51], v[50:51], v[54:55]
	v_cmp_lt_u32_e64 s[10:11], s10, v136
	v_pk_mul_f32 v[54:55], v[52:53], v[56:57]
	v_pk_mul_f32 v[52:53], v[50:51], v[58:59] op_sel_hi:[1,0]
	v_pk_mul_f32 v[50:51], v[54:55], v[58:59] op_sel_hi:[1,0]
	s_and_saveexec_b64 s[12:13], s[10:11]
	s_xor_b64 s[12:13], exec, s[12:13]
	s_cbranch_execz .LBB0_291
	v_cmp_lt_u32_e32 vcc, s95, v136
	s_and_saveexec_b64 s[16:17], vcc
	s_xor_b64 s[16:17], exec, s[16:17]
	s_cbranch_execz .LBB0_288
	v_cmp_lt_u32_e32 vcc, s96, v136
	s_and_saveexec_b64 s[76:77], vcc
	s_xor_b64 s[76:77], exec, s[76:77]
	s_cbranch_execz .LBB0_285
	v_cmp_gt_u32_e32 vcc, s97, v136
	s_and_saveexec_b64 s[78:79], vcc
	s_cbranch_execz .LBB0_284
	v_lshl_add_u64 v[54:55], v[136:137], 2, s[30:31]
	v_lshl_add_u64 v[56:57], v[54:55], 0, v[94:95]
	v_add_co_u32_e32 v56, vcc, 0xffffc000, v56
	s_nop 1
	v_addc_co_u32_e32 v57, vcc, -1, v57, vcc
	global_store_dword v[56:57], v52, off offset:-1856
	v_lshl_add_u64 v[56:57], v[54:55], 0, v[92:93]
	v_add_co_u32_e32 v56, vcc, 0xffffc000, v56
	s_nop 1
	v_addc_co_u32_e32 v57, vcc, -1, v57, vcc
	global_store_dword v[56:57], v53, off offset:-1856
	v_lshl_add_u64 v[52:53], v[54:55], 0, v[88:89]
	v_add_co_u32_e32 v52, vcc, 0xffffc000, v52
	s_nop 1
	v_addc_co_u32_e32 v53, vcc, -1, v53, vcc
	global_store_dword v[52:53], v50, off offset:-1856
	v_lshl_add_u64 v[52:53], v[54:55], 0, v[84:85]
	v_add_co_u32_e32 v52, vcc, 0xffffc000, v52
	s_nop 1
	v_addc_co_u32_e32 v53, vcc, -1, v53, vcc
	global_store_dword v[52:53], v51, off offset:-1856

; template <bool I8 = false, class Epi> ...
;     ...
; #pragma unroll
;   for (int i = 0; i < 4; ++i) {
;     const int row = m0 + wm * 64 + i * 16 + (lane >> 4) * 4;
;     float4 rs = float4{1.f, 1.f, 1.f, 1.f};
;     if (I8) rs = *reinterpret_cast<const float4*>(rscale + row);
; #pragma unroll
;     for (int j = 0; j < 4; ++j) {
;       const int col = n0 + wn * 64 + j * 16 + (lane & 15);
;       if (I8) {
;         typedef __attribute__((ext_vector_type(4))) int i32x4;
;         const i32x4 ia = __builtin_bit_cast(i32x4, acc[i][j]);
;         const float cs = cscale[col];
;         epi(row, col, f32x4{(float)ia[0] * rs.x * cs, (float)ia[1] * rs.y * cs, (float)ia[2] * rs.z * cs, (float)ia[3] * rs.w * cs});
;       } else {
;         epi(row, col, acc[i][j]);
;       }
;     }
;   __device__ __forceinline__ void operator()(int row, int col, f32x4 v) const {
;     if (col < 2048) {
;       int ch = col & 1023, half = col >> 10;
;       int b = row / seqlen, l = row - b * seqlen;
;       uint2 pk; pk.x = pack2(v[0], v[1]); pk.y = pack2(v[2], v[3]);
;       *reinterpret_cast<uint2*>(ABt + ((size_t)(b * 1024 + ch) * 4096 + half * 2048 + l)) = pk;
;     } else if (col < 3072) {
; #pragma unroll
;       for (int r = 0; r < 4; ++r) z[(size_t)(row + r) * 1024 + (col - 2048)] = f2bf(v[r]);
;     } else if (col < 4608) {
; #pragma unroll
;       for (int r = 0; r < 4; ++r) xbcraw[(size_t)(row + r) * DXBC + (col - 3072)] = f2bf(v[r]);
;     } else if (col < 4640) {
; #pragma unroll
;       for (int r = 0; r < 4; ++r) dtraw[(size_t)(row + r) * 32 + (col - 4608)] = v[r];
;     }
;   }
.LBB0_293:
	s_or_b64 exec, exec, s[12:13]
	v_or_b32_e32 v54, 16, v78
	v_ashrrev_i32_e32 v55, 31, v54
	v_lshl_add_u64 v[50:51], v[54:55], 2, s[52:53]
	v_mov_b32_e32 v50, v212
	v_mov_b32_e32 v51, v213
	v_mov_b32_e32 v52, v214
	v_mov_b32_e32 v53, v215
	v_cvt_f32_i32_e32 v89, v47
	v_cvt_f32_i32_e32 v88, v46
	v_cvt_f32_i32_e32 v91, v49
	v_cvt_f32_i32_e32 v90, v48
	v_or_b32_e32 v70, 17, v78
	v_or_b32_e32 v86, 19, v78
	v_or_b32_e32 v74, 18, v78
	v_ashrrev_i32_e32 v71, 31, v70
	v_ashrrev_i32_e32 v87, 31, v86
	v_mov_b32_e32 v81, v80
	v_cndmask_b32_e64 v59, 0, 1, s[14:15]
	v_ashrrev_i32_e32 v75, 31, v74
	v_mad_i64_i32 v[64:65], s[12:13], v54, s83, 0
	v_mad_i64_i32 v[56:57], s[12:13], v70, s83, 0
	v_mad_i64_i32 v[48:49], s[12:13], v74, s83, 0
	v_mad_i64_i32 v[46:47], s[12:13], v86, s83, 0
	v_lshlrev_b64 v[72:73], 7, v[70:71]
	v_lshlrev_b64 v[60:61], 7, v[86:87]
	v_lshlrev_b64 v[76:77], 11, v[70:71]
	v_lshlrev_b64 v[70:71], 11, v[86:87]
	v_cmp_ne_u32_e64 s[12:13], 1, v59
	v_lshlrev_b64 v[82:83], 7, v[54:55]
	v_lshlrev_b64 v[68:69], 7, v[74:75]
	v_lshlrev_b64 v[84:85], 11, v[54:55]
	v_lshlrev_b64 v[74:75], 11, v[74:75]
	s_andn2_b64 vcc, exec, s[14:15]
	s_mov_b64 s[14:15], -1
	v_pk_mul_f32 v[86:87], v[50:51], v[88:89]
	v_pk_mul_f32 v[88:89], v[52:53], v[90:91]
	v_pk_mul_f32 v[86:87], v[80:81], v[86:87]
	v_pk_mul_f32 v[88:89], v[80:81], v[88:89]
	s_cbranch_vccnz .LBB0_305
	s_cmp_gt_u32 s94, 0xfffff3ff
	s_cbranch_scc1 .LBB0_302
	s_cmpk_lt_u32 s91, 0x1200
	s_cbranch_scc1 .LBB0_299
	v_cmp_gt_u32_e32 vcc, s85, v136
	s_and_saveexec_b64 s[14:15], vcc
	s_cbranch_execz .LBB0_298
	v_lshl_add_u64 v[90:91], v[136:137], 2, s[30:31]
	v_lshl_add_u64 v[92:93], v[90:91], 0, v[82:83]
	v_add_co_u32_e32 v92, vcc, 0xffffc000, v92
	s_nop 1
	v_addc_co_u32_e32 v93, vcc, -1, v93, vcc
	global_store_dword v[92:93], v86, off offset:-2048
	v_lshl_add_u64 v[92:93], v[90:91], 0, v[72:73]
	v_add_co_u32_e32 v92, vcc, 0xffffc000, v92
	s_nop 1
	v_addc_co_u32_e32 v93, vcc, -1, v93, vcc
	global_store_dword v[92:93], v87, off offset:-2048
	v_lshl_add_u64 v[92:93], v[90:91], 0, v[68:69]
	v_add_co_u32_e32 v92, vcc, 0xffffc000, v92
	v_lshl_add_u64 v[90:91], v[90:91], 0, v[60:61]
	s_nop 0
	v_addc_co_u32_e32 v93, vcc, -1, v93, vcc
	v_add_co_u32_e32 v90, vcc, 0xffffc000, v90
	global_store_dword v[92:93], v88, off offset:-2048
	s_nop 0
	v_addc_co_u32_e32 v91, vcc, -1, v91, vcc
	global_store_dword v[90:91], v89, off offset:-2048

; template <bool I8 = false, class Epi> ...
;     ...
; #pragma unroll
;   for (int i = 0; i < 4; ++i) {
;     const int row = m0 + wm * 64 + i * 16 + (lane >> 4) * 4;
;     float4 rs = float4{1.f, 1.f, 1.f, 1.f};
;     if (I8) rs = *reinterpret_cast<const float4*>(rscale + row);
; #pragma unroll
;     for (int j = 0; j < 4; ++j) {
;       const int col = n0 + wn * 64 + j * 16 + (lane & 15);
;       if (I8) {
;         typedef __attribute__((ext_vector_type(4))) int i32x4;
;         const i32x4 ia = __builtin_bit_cast(i32x4, acc[i][j]);
;         const float cs = cscale[col];
;         epi(row, col, f32x4{(float)ia[0] * rs.x * cs, (float)ia[1] * rs.y * cs, (float)ia[2] * rs.z * cs, (float)ia[3] * rs.w * cs});
;       } else {
;         epi(row, col, acc[i][j]);
;       }
;     }
;   __device__ __forceinline__ void operator()(int row, int col, f32x4 v) const {
;     if (col < 2048) {
;       int ch = col & 1023, half = col >> 10;
;       int b = row / seqlen, l = row - b * seqlen;
;       uint2 pk; pk.x = pack2(v[0], v[1]); pk.y = pack2(v[2], v[3]);
;       *reinterpret_cast<uint2*>(ABt + ((size_t)(b * 1024 + ch) * 4096 + half * 2048 + l)) = pk;
;     } else if (col < 3072) {
; #pragma unroll
;       for (int r = 0; r < 4; ++r) z[(size_t)(row + r) * 1024 + (col - 2048)] = f2bf(v[r]);
;     } else if (col < 4608) {
; #pragma unroll
;       for (int r = 0; r < 4; ++r) xbcraw[(size_t)(row + r) * DXBC + (col - 3072)] = f2bf(v[r]);
;     } else if (col < 4640) {
; #pragma unroll
;       for (int r = 0; r < 4; ++r) dtraw[(size_t)(row + r) * 32 + (col - 4608)] = v[r];
;     }
;   }
.LBB0_348:
	s_or_b64 exec, exec, s[14:15]
	v_or_b32_e32 v38, 32, v78
	v_ashrrev_i32_e32 v39, 31, v38
	v_lshl_add_u64 v[34:35], v[38:39], 2, s[52:53]
	v_mov_b32_e32 v34, v216
	v_mov_b32_e32 v35, v217
	v_mov_b32_e32 v36, v218
	v_mov_b32_e32 v37, v219
	v_cvt_f32_i32_e32 v69, v31
	v_cvt_f32_i32_e32 v68, v30
	v_cvt_f32_i32_e32 v71, v33
	v_cvt_f32_i32_e32 v70, v32
	v_or_b32_e32 v48, 33, v78
	v_or_b32_e32 v64, 35, v78
	v_or_b32_e32 v52, 34, v78
	v_ashrrev_i32_e32 v49, 31, v48
	v_ashrrev_i32_e32 v65, 31, v64
	v_ashrrev_i32_e32 v53, 31, v52
	v_mad_i64_i32 v[44:45], s[14:15], v38, s83, 0
	v_mad_i64_i32 v[40:41], s[14:15], v48, s83, 0
	v_mad_i64_i32 v[32:33], s[14:15], v52, s83, 0
	v_mad_i64_i32 v[30:31], s[14:15], v64, s83, 0
	v_lshlrev_b64 v[50:51], 7, v[48:49]
	v_lshlrev_b64 v[42:43], 7, v[64:65]
	v_lshlrev_b64 v[54:55], 11, v[48:49]
	v_lshlrev_b64 v[48:49], 11, v[64:65]
	s_and_b64 vcc, exec, s[12:13]
	v_lshlrev_b64 v[56:57], 7, v[38:39]
	v_lshlrev_b64 v[46:47], 7, v[52:53]
	v_lshlrev_b64 v[60:61], 11, v[38:39]
	v_lshlrev_b64 v[52:53], 11, v[52:53]
	s_mov_b64 s[14:15], -1
	v_pk_mul_f32 v[64:65], v[34:35], v[68:69]
	v_pk_mul_f32 v[68:69], v[36:37], v[70:71]
	v_pk_mul_f32 v[64:65], v[80:81], v[64:65]
	v_pk_mul_f32 v[68:69], v[80:81], v[68:69]
	s_cbranch_vccnz .LBB0_360
	s_cmp_gt_u32 s94, 0xfffff3ff
	s_cbranch_scc1 .LBB0_357
	s_cmpk_lt_u32 s91, 0x1200
	s_cbranch_scc1 .LBB0_354
	v_cmp_gt_u32_e32 vcc, s85, v136
	s_and_saveexec_b64 s[14:15], vcc
	s_cbranch_execz .LBB0_353
	v_lshl_add_u64 v[70:71], v[136:137], 2, s[30:31]
	v_lshl_add_u64 v[72:73], v[70:71], 0, v[56:57]
	v_add_co_u32_e32 v72, vcc, 0xffffc000, v72
	s_nop 1
	v_addc_co_u32_e32 v73, vcc, -1, v73, vcc
	global_store_dword v[72:73], v64, off offset:-2048
	v_lshl_add_u64 v[72:73], v[70:71], 0, v[50:51]
	v_add_co_u32_e32 v72, vcc, 0xffffc000, v72
	s_nop 1
	v_addc_co_u32_e32 v73, vcc, -1, v73, vcc
	global_store_dword v[72:73], v65, off offset:-2048
	v_lshl_add_u64 v[72:73], v[70:71], 0, v[46:47]
	v_add_co_u32_e32 v72, vcc, 0xffffc000, v72
	v_lshl_add_u64 v[70:71], v[70:71], 0, v[42:43]
	s_nop 0
	v_addc_co_u32_e32 v73, vcc, -1, v73, vcc
	v_add_co_u32_e32 v70, vcc, 0xffffc000, v70
	global_store_dword v[72:73], v68, off offset:-2048
	s_nop 0
	v_addc_co_u32_e32 v71, vcc, -1, v71, vcc
	global_store_dword v[70:71], v69, off offset:-2048

; template <bool I8 = false, class Epi> ...
;     ...
; #pragma unroll
;   for (int i = 0; i < 4; ++i) {
;     const int row = m0 + wm * 64 + i * 16 + (lane >> 4) * 4;
;     float4 rs = float4{1.f, 1.f, 1.f, 1.f};
;     if (I8) rs = *reinterpret_cast<const float4*>(rscale + row);
; #pragma unroll
;     for (int j = 0; j < 4; ++j) {
;       const int col = n0 + wn * 64 + j * 16 + (lane & 15);
;       if (I8) {
;         typedef __attribute__((ext_vector_type(4))) int i32x4;
;         const i32x4 ia = __builtin_bit_cast(i32x4, acc[i][j]);
;         const float cs = cscale[col];
;         epi(row, col, f32x4{(float)ia[0] * rs.x * cs, (float)ia[1] * rs.y * cs, (float)ia[2] * rs.z * cs, (float)ia[3] * rs.w * cs});
;       } else {
;         epi(row, col, acc[i][j]);
;       }
;     }
;   __device__ __forceinline__ void operator()(int row, int col, f32x4 v) const {
;     if (col < 2048) {
;       int ch = col & 1023, half = col >> 10;
;       int b = row / seqlen, l = row - b * seqlen;
;       uint2 pk; pk.x = pack2(v[0], v[1]); pk.y = pack2(v[2], v[3]);
;       *reinterpret_cast<uint2*>(ABt + ((size_t)(b * 1024 + ch) * 4096 + half * 2048 + l)) = pk;
;     } else if (col < 3072) {
; #pragma unroll
;       for (int r = 0; r < 4; ++r) z[(size_t)(row + r) * 1024 + (col - 2048)] = f2bf(v[r]);
;     } else if (col < 4608) {
; #pragma unroll
;       for (int r = 0; r < 4; ++r) xbcraw[(size_t)(row + r) * DXBC + (col - 3072)] = f2bf(v[r]);
;     } else if (col < 4640) {
; #pragma unroll
;       for (int r = 0; r < 4; ++r) dtraw[(size_t)(row + r) * 32 + (col - 4608)] = v[r];
;     }
;   }
.LBB0_403:
	s_or_b64 exec, exec, s[14:15]
	v_or_b32_e32 v22, 48, v78
	v_ashrrev_i32_e32 v23, 31, v22
	v_lshl_add_u64 v[18:19], v[22:23], 2, s[52:53]
	v_mov_b32_e32 v18, v220
	v_mov_b32_e32 v19, v221
	v_mov_b32_e32 v20, v222
	v_mov_b32_e32 v21, v223
	v_cvt_f32_i32_e32 v47, v15
	v_cvt_f32_i32_e32 v46, v14
	v_cvt_f32_i32_e32 v49, v17
	v_cvt_f32_i32_e32 v48, v16
	v_or_b32_e32 v32, 49, v78
	v_or_b32_e32 v44, 51, v78
	v_or_b32_e32 v36, 50, v78
	v_ashrrev_i32_e32 v33, 31, v32
	v_ashrrev_i32_e32 v45, 31, v44
	s_and_b64 vcc, exec, s[12:13]
	v_ashrrev_i32_e32 v37, 31, v36
	v_mad_i64_i32 v[28:29], s[12:13], v22, s83, 0
	v_mad_i64_i32 v[24:25], s[12:13], v32, s83, 0
	v_mad_i64_i32 v[16:17], s[12:13], v36, s83, 0
	v_mad_i64_i32 v[14:15], s[12:13], v44, s83, 0
	v_lshlrev_b64 v[34:35], 7, v[32:33]
	v_lshlrev_b64 v[26:27], 7, v[44:45]
	v_lshlrev_b64 v[38:39], 11, v[32:33]
	v_lshlrev_b64 v[32:33], 11, v[44:45]
	v_lshlrev_b64 v[40:41], 7, v[22:23]
	v_lshlrev_b64 v[30:31], 7, v[36:37]
	v_lshlrev_b64 v[42:43], 11, v[22:23]
	v_lshlrev_b64 v[36:37], 11, v[36:37]
	s_mov_b64 s[12:13], -1
	v_pk_mul_f32 v[44:45], v[18:19], v[46:47]
	v_pk_mul_f32 v[46:47], v[20:21], v[48:49]
	v_pk_mul_f32 v[44:45], v[80:81], v[44:45]
	v_pk_mul_f32 v[46:47], v[80:81], v[46:47]
	s_cbranch_vccnz .LBB0_415
	s_cmp_gt_u32 s94, 0xfffff3ff
	s_cbranch_scc1 .LBB0_412
	s_cmpk_lt_u32 s91, 0x1200
	s_cbranch_scc1 .LBB0_409
	v_cmp_gt_u32_e32 vcc, s85, v136
	s_and_saveexec_b64 s[12:13], vcc
	s_cbranch_execz .LBB0_408
	v_lshl_add_u64 v[48:49], v[136:137], 2, s[30:31]
	v_lshl_add_u64 v[50:51], v[48:49], 0, v[40:41]
	v_add_co_u32_e32 v50, vcc, 0xffffc000, v50
	s_nop 1
	v_addc_co_u32_e32 v51, vcc, -1, v51, vcc
	global_store_dword v[50:51], v44, off offset:-2048
	v_lshl_add_u64 v[50:51], v[48:49], 0, v[34:35]
	v_add_co_u32_e32 v50, vcc, 0xffffc000, v50
	s_nop 1
	v_addc_co_u32_e32 v51, vcc, -1, v51, vcc
	global_store_dword v[50:51], v45, off offset:-2048
	v_lshl_add_u64 v[50:51], v[48:49], 0, v[30:31]
	v_add_co_u32_e32 v50, vcc, 0xffffc000, v50
	v_lshl_add_u64 v[48:49], v[48:49], 0, v[26:27]
	s_nop 0
	v_addc_co_u32_e32 v51, vcc, -1, v51, vcc
	v_add_co_u32_e32 v48, vcc, 0xffffc000, v48
	global_store_dword v[50:51], v46, off offset:-2048
	s_nop 0
	v_addc_co_u32_e32 v49, vcc, -1, v49, vcc
	global_store_dword v[48:49], v47, off offset:-2048

; template <bool I8 = false>
; __device__ __forceinline__ void gemm_mainloop(const bf16_t* __restrict__ A, int lda, const bf16_t* __restrict__ Bt, int ldb,
;                                               int K, int m0, int n0, f32x4 (&acc)[4][4], char* smem) {
;     ...
;   for (int kt = 0; kt < nk; ++kt) {
;     const int cur = kt & 1;
;     if (kt + 1 < nk) GSTAGE(cur ^ 1, kt + 1);
;     const char* sA = smem + cur * 32768;
;     const char* sB = sA + 16384;
; #pragma unroll
;     for (int kk = 0; kk < 2; ++kk) {
;       bf16x8 af[4], bfr[4];
;       const int ch = kk * 4 + (lane >> 4);
; #pragma unroll
;       for (int i = 0; i < 4; ++i) {
;         int row = wm * 64 + i * 16 + (lane & 15);
;         af[i] = *reinterpret_cast<const bf16x8*>(sA + row * 128 + ((ch ^ (row & 7)) << 4));
;         int col = wn * 64 + i * 16 + (lane & 15);
;         bfr[i] = *reinterpret_cast<const bf16x8*>(sB + col * 128 + ((ch ^ (col & 7)) << 4));
;       }
; #pragma unroll
;       for (int i = 0; i < 4; ++i)
; #pragma unroll
;         for (int j = 0; j < 4; ++j) {
;           if (I8) {
;             typedef __attribute__((ext_vector_type(4))) int i32x4;
;             acc[i][j] = __builtin_bit_cast(f32x4, __builtin_amdgcn_mfma_i32_16x16x64_i8(__builtin_bit_cast(i32x4, af[i]), __builtin_bit_cast(i32x4, bfr[j]),
;                                                                                          __builtin_bit_cast(i32x4, acc[i][j]), 0, 0, 0));
;           } else {
;             acc[i][j] = __builtin_amdgcn_mfma_f32_16x16x32_bf16(af[i], bfr[j], acc[i][j], 0, 0, 0);
;           }
;         }
;     }
;     asm volatile("s_waitcnt vmcnt(0)" ::: "memory");
;     __syncthreads();
;   }
.LBB0_461:
	s_and_b32 s12, s11, 0x8000
	s_xor_b32 s13, s12, 0x8000
	v_add_u32_e32 v92, s13, v73
	v_lshl_add_u64 v[76:77], v[68:69], 0, s[6:7]
	v_readfirstlane_b32 s13, v92
	v_add_u32_e32 v93, 0x4000, v92
	v_lshl_add_u64 v[78:79], v[66:67], 0, s[6:7]
	v_lshl_add_u64 v[80:81], v[76:77], 0, s[60:61]
	v_add_u32_e32 v94, 0x1000, v92
	v_readfirstlane_b32 s14, v93
	s_mov_b32 m0, s13
	v_lshl_add_u64 v[82:83], v[78:79], 0, s[60:61]
	v_add_u32_e32 v95, 0x5000, v92
	v_readfirstlane_b32 s15, v94
	global_load_lds_dwordx4 v[80:81], off
	s_mov_b32 m0, s14
	v_lshl_add_u64 v[84:85], v[76:77], 0, s[62:63]
	v_add_u32_e32 v97, 0x2000, v92
	v_readfirstlane_b32 s16, v95
	global_load_lds_dwordx4 v[82:83], off
	s_mov_b32 m0, s15
	v_lshl_add_u64 v[86:87], v[78:79], 0, s[62:63]
	v_add_u32_e32 v98, 0x6000, v92
	v_readfirstlane_b32 s17, v97
	global_load_lds_dwordx4 v[84:85], off
	s_mov_b32 m0, s16
	v_lshl_add_u64 v[88:89], v[76:77], 0, s[64:65]
	v_add_u32_e32 v99, 0x3000, v92
	v_readfirstlane_b32 s76, v98
	global_load_lds_dwordx4 v[86:87], off
	s_mov_b32 m0, s17
	v_lshl_add_u64 v[90:91], v[78:79], 0, s[64:65]
	v_add_u32_e32 v92, 0x7000, v92
	v_readfirstlane_b32 s77, v99
	global_load_lds_dwordx4 v[88:89], off
	s_mov_b32 m0, s76
	v_lshl_add_u64 v[76:77], v[76:77], 0, s[66:67]
	v_readfirstlane_b32 s78, v92
	global_load_lds_dwordx4 v[90:91], off
	s_mov_b32 m0, s77
	v_lshl_add_u64 v[78:79], v[78:79], 0, s[66:67]
	global_load_lds_dwordx4 v[76:77], off
	s_mov_b32 m0, s78
	v_or_b32_e32 v75, s12, v74
	global_load_lds_dwordx4 v[78:79], off
	v_add_u32_e32 v96, v75, v72
	v_add_u32_e32 v75, v75, v70
	ds_read_b128 v[76:79], v96
	ds_read_b128 v[80:83], v75 offset:16384
	ds_read_b128 v[84:87], v75 offset:18432
	ds_read_b128 v[88:91], v75 offset:20480
	ds_read_b128 v[92:95], v75 offset:22528
	s_waitcnt lgkmcnt(0)
	v_mfma_i32_16x16x64_i8 v[62:65], v[76:79], v[80:83], v[62:65]
	v_or_b32_e32 v75, s12, v71
	s_add_i32 s11, s11, 0x8000
	s_add_u32 s6, s6, 0x80
	v_mfma_i32_16x16x64_i8 v[58:61], v[76:79], v[84:87], v[58:61]
	s_addc_u32 s7, s7, 0
	s_cmpk_lg_i32 s6, 0x780
	v_mfma_i32_16x16x64_i8 v[54:57], v[76:79], v[88:91], v[54:57]
	v_mfma_i32_16x16x64_i8 v[46:49], v[76:79], v[92:95], v[46:49]
	ds_read_b128 v[76:79], v96 offset:2048
	s_waitcnt lgkmcnt(0)
	v_mfma_i32_16x16x64_i8 v[38:41], v[76:79], v[80:83], v[38:41]
	v_mfma_i32_16x16x64_i8 v[34:37], v[76:79], v[84:87], v[34:37]
	v_mfma_i32_16x16x64_i8 v[30:33], v[76:79], v[88:91], v[30:33]
	v_mfma_i32_16x16x64_i8 v[26:29], v[76:79], v[92:95], v[26:29]
	ds_read_b128 v[76:79], v96 offset:4096
	s_waitcnt lgkmcnt(0)
	v_mfma_i32_16x16x64_i8 v[22:25], v[76:79], v[80:83], v[22:25]
	v_mfma_i32_16x16x64_i8 v[18:21], v[76:79], v[84:87], v[18:21]
	v_mfma_i32_16x16x64_i8 v[14:17], v[76:79], v[88:91], v[14:17]
	v_mfma_i32_16x16x64_i8 v[10:13], v[76:79], v[92:95], v[10:13]
	ds_read_b128 v[76:79], v96 offset:6144
	v_add_u32_e32 v96, v75, v72
	v_add_u32_e32 v75, v75, v70
	s_waitcnt lgkmcnt(0)
	v_mfma_i32_16x16x64_i8 v[6:9], v[76:79], v[80:83], v[6:9]
	ds_read_b128 v[80:83], v96
	v_mfma_i32_16x16x64_i8 v[2:5], v[76:79], v[84:87], v[2:5]
	ds_read_b128 v[84:87], v75 offset:18432
	v_mfma_i32_16x16x64_i8 v[50:53], v[76:79], v[88:91], v[50:53]
	ds_read_b128 v[88:91], v75 offset:20480
	v_mfma_i32_16x16x64_i8 v[42:45], v[76:79], v[92:95], v[42:45]
	ds_read_b128 v[76:79], v75 offset:16384
	ds_read_b128 v[92:95], v75 offset:22528
	s_waitcnt lgkmcnt(0)
	v_mfma_i32_16x16x64_i8 v[62:65], v[80:83], v[76:79], v[62:65]
	v_mfma_i32_16x16x64_i8 v[58:61], v[80:83], v[84:87], v[58:61]
	v_mfma_i32_16x16x64_i8 v[54:57], v[80:83], v[88:91], v[54:57]
	v_mfma_i32_16x16x64_i8 v[46:49], v[80:83], v[92:95], v[46:49]
	ds_read_b128 v[80:83], v96 offset:2048
	s_waitcnt lgkmcnt(0)
	v_mfma_i32_16x16x64_i8 v[38:41], v[80:83], v[76:79], v[38:41]
	v_mfma_i32_16x16x64_i8 v[34:37], v[80:83], v[84:87], v[34:37]
	v_mfma_i32_16x16x64_i8 v[30:33], v[80:83], v[88:91], v[30:33]
	v_mfma_i32_16x16x64_i8 v[26:29], v[80:83], v[92:95], v[26:29]
	ds_read_b128 v[80:83], v96 offset:4096
	s_waitcnt lgkmcnt(0)
	v_mfma_i32_16x16x64_i8 v[22:25], v[80:83], v[76:79], v[22:25]
	v_mfma_i32_16x16x64_i8 v[18:21], v[80:83], v[84:87], v[18:21]
	v_mfma_i32_16x16x64_i8 v[14:17], v[80:83], v[88:91], v[14:17]
	v_mfma_i32_16x16x64_i8 v[10:13], v[80:83], v[92:95], v[10:13]
	ds_read_b128 v[80:83], v96 offset:6144
	s_waitcnt vmcnt(0)
	s_waitcnt vmcnt(0) lgkmcnt(0)
	v_mfma_i32_16x16x64_i8 v[6:9], v[80:83], v[76:79], v[6:9]
	s_barrier
	v_mfma_i32_16x16x64_i8 v[2:5], v[80:83], v[84:87], v[2:5]
	v_mfma_i32_16x16x64_i8 v[50:53], v[80:83], v[88:91], v[50:53]
	v_mfma_i32_16x16x64_i8 v[42:45], v[80:83], v[92:95], v[42:45]
	s_cbranch_scc1 .LBB0_461
; template <bool I8 = false, class Epi> ...
;     ...
;   gemm_mainloop<I8>(A, lda, Bt, ldb, K, m0, n0, acc, smem);
; #pragma unroll
;   for (int i = 0; i < 4; ++i) {
;     const int row = m0 + wm * 64 + i * 16 + (lane >> 4) * 4;
;     float4 rs = float4{1.f, 1.f, 1.f, 1.f};
;     if (I8) rs = *reinterpret_cast<const float4*>(rscale + row);
; #pragma unroll
;     for (int j = 0; j < 4; ++j) {
;       const int col = n0 + wn * 64 + j * 16 + (lane & 15);
;       if (I8) {
;         typedef __attribute__((ext_vector_type(4))) int i32x4;
;         const i32x4 ia = __builtin_bit_cast(i32x4, acc[i][j]);
;         const float cs = cscale[col];
;         epi(row, col, f32x4{(float)ia[0] * rs.x * cs, (float)ia[1] * rs.y * cs, (float)ia[2] * rs.z * cs, (float)ia[3] * rs.w * cs});
;       } else {
;         epi(row, col, acc[i][j]);
;       }
;     }
;   __device__ __forceinline__ void operator()(int row, int col, f32x4 v) const {
;     if (col < 2048) {
;       int ch = col & 1023, half = col >> 10;
;       int b = row / seqlen, l = row - b * seqlen;
;       uint2 pk; pk.x = pack2(v[0], v[1]); pk.y = pack2(v[2], v[3]);
;       *reinterpret_cast<uint2*>(ABt + ((size_t)(b * 1024 + ch) * 4096 + half * 2048 + l)) = pk;
;     } else if (col < 3072) {
; #pragma unroll
;       for (int r = 0; r < 4; ++r) z[(size_t)(row + r) * 1024 + (col - 2048)] = f2bf(v[r]);
;     } else if (col < 4608) {
; #pragma unroll
;       for (int r = 0; r < 4; ++r) xbcraw[(size_t)(row + r) * DXBC + (col - 3072)] = f2bf(v[r]);
;     } else if (col < 4640) {
; #pragma unroll
;       for (int r = 0; r < 4; ++r) dtraw[(size_t)(row + r) * 32 + (col - 4608)] = v[r];
;     }
;   }
	v_add_u32_e32 v73, v74, v72
	ds_read_b128 v[66:69], v73 offset:32768
	v_add_u32_e32 v86, v74, v70
	ds_read_b128 v[74:77], v86 offset:49152
	ds_read_b128 v[78:81], v86 offset:51200
	ds_read_b128 v[82:85], v86 offset:53248
	ds_read_b128 v[86:89], v86 offset:55296
	v_add_u32_e32 v72, v71, v72
	v_or_b32_e32 v92, s10, v164
	s_cmpk_lt_u32 s8, 0xa00
	s_waitcnt lgkmcnt(3)
	v_mfma_i32_16x16x64_i8 v[62:65], v[66:69], v[74:77], v[62:65]
	s_cselect_b64 s[12:13], -1, 0
	s_cmpk_gt_u32 s8, 0x9ff
	s_cselect_b64 s[76:77], -1, 0
	s_waitcnt lgkmcnt(2)
	v_mfma_i32_16x16x64_i8 v[58:61], v[66:69], v[78:81], v[58:61]
	s_and_b64 vcc, exec, s[76:77]
	v_cmp_gt_u32_e64 s[6:7], s85, v92
	s_waitcnt lgkmcnt(1)
	v_mfma_i32_16x16x64_i8 v[54:57], v[66:69], v[82:85], v[54:57]
	s_waitcnt lgkmcnt(0)
	v_mfma_i32_16x16x64_i8 v[46:49], v[66:69], v[86:89], v[46:49]
	ds_read_b128 v[66:69], v73 offset:34816
	s_waitcnt lgkmcnt(0)
	v_mfma_i32_16x16x64_i8 v[38:41], v[66:69], v[74:77], v[38:41]
	v_mfma_i32_16x16x64_i8 v[34:37], v[66:69], v[78:81], v[34:37]
	v_mfma_i32_16x16x64_i8 v[30:33], v[66:69], v[82:85], v[30:33]
	v_mfma_i32_16x16x64_i8 v[26:29], v[66:69], v[86:89], v[26:29]
	ds_read_b128 v[66:69], v73 offset:36864
	s_waitcnt lgkmcnt(0)
	v_mfma_i32_16x16x64_i8 v[22:25], v[66:69], v[74:77], v[22:25]
	v_mfma_i32_16x16x64_i8 v[18:21], v[66:69], v[78:81], v[18:21]
	v_mfma_i32_16x16x64_i8 v[14:17], v[66:69], v[82:85], v[14:17]
	v_mfma_i32_16x16x64_i8 v[10:13], v[66:69], v[86:89], v[10:13]
	ds_read_b128 v[66:69], v73 offset:38912
	s_waitcnt lgkmcnt(0)
	v_mfma_i32_16x16x64_i8 v[96:99], v[66:69], v[82:85], v[50:53]
	s_nop 2
	ds_read_b128 v[50:53], v72 offset:32768
	v_mfma_i32_16x16x64_i8 v[84:87], v[66:69], v[86:89], v[42:45]
	s_nop 2
	v_add_u32_e32 v42, v71, v70
	ds_read_b128 v[100:103], v42 offset:49152
	ds_read_b128 v[88:91], v72 offset:34816
	ds_read_b128 v[104:107], v42 offset:51200
	ds_read_b128 v[112:115], v42 offset:53248
	v_mfma_i32_16x16x64_i8 v[6:9], v[66:69], v[74:77], v[6:9]
	ds_read_b128 v[116:119], v72 offset:36864
	ds_read_b128 v[120:123], v72 offset:38912
	ds_read_b128 v[124:127], v42 offset:55296
	s_waitcnt vmcnt(0)
	s_waitcnt lgkmcnt(0)
	v_mfma_i32_16x16x64_i8 v[2:5], v[66:69], v[78:81], v[2:5]
	v_add_u32_e32 v68, s9, v145
	v_ashrrev_i32_e32 v69, 31, v68
	v_lshl_add_u64 v[70:71], v[68:69], 2, s[24:25]
	v_mfma_i32_16x16x64_i8 v[108:111], v[50:53], v[100:103], v[62:65]
	s_barrier
	v_lshlrev_b32_e32 v66, 2, v92
	v_mfma_i32_16x16x64_i8 v[62:65], v[50:53], v[104:107], v[58:61]
	global_load_dword v93, v66, s[26:27]
	v_lshlrev_b64 v[78:79], 7, v[68:69]
	v_or_b32_e32 v72, 1, v68
	v_mfma_i32_16x16x64_i8 v[58:61], v[50:53], v[112:115], v[54:57]
	v_ashrrev_i32_e32 v73, 31, v72
	v_lshlrev_b64 v[76:77], 7, v[72:73]
	v_or_b32_e32 v82, 2, v68
	global_load_dwordx4 v[54:57], v[70:71], off
	global_load_dwordx4 v[212:215], v[70:71], off offset:64
	global_load_dwordx4 v[216:219], v[70:71], off offset:128
	global_load_dwordx4 v[220:223], v[70:71], off offset:192
	global_load_dword v225, v66, s[26:27] offset:64
	global_load_dword v226, v66, s[26:27] offset:128
	global_load_dword v227, v66, s[26:27] offset:192
	v_mfma_i32_16x16x64_i8 v[50:53], v[50:53], v[124:127], v[46:49]
	v_ashrrev_i32_e32 v83, 31, v82
	v_lshlrev_b64 v[74:75], 7, v[82:83]
	s_mov_b64 s[8:9], -1
	v_mfma_i32_16x16x64_i8 v[46:49], v[88:91], v[100:103], v[38:41]
	v_mfma_i32_16x16x64_i8 v[38:41], v[88:91], v[112:115], v[30:33]
	v_mfma_i32_16x16x64_i8 v[30:33], v[116:119], v[100:103], v[22:25]
	s_nop 2
	v_cvt_f32_i32_e32 v22, v108
	v_mfma_i32_16x16x64_i8 v[42:45], v[88:91], v[104:107], v[34:37]
	v_mfma_i32_16x16x64_i8 v[34:37], v[88:91], v[124:127], v[26:29]
	v_or_b32_e32 v90, 3, v68
	v_ashrrev_i32_e32 v91, 31, v90
	v_lshlrev_b64 v[80:81], 7, v[90:91]
	v_mfma_i32_16x16x64_i8 v[26:29], v[116:119], v[104:107], v[18:21]
	s_nop 2
	v_cvt_f32_i32_e32 v18, v109
	s_waitcnt vmcnt(0)
	v_mul_f32_e32 v19, v54, v22
	v_mul_f32_e32 v69, v19, v93
	v_mfma_i32_16x16x64_i8 v[22:25], v[116:119], v[112:115], v[14:17]
	s_nop 2
	v_mul_f32_e32 v14, v55, v18
	v_cvt_f32_i32_e32 v15, v110
	v_mfma_i32_16x16x64_i8 v[18:21], v[116:119], v[124:127], v[10:13]
	v_mul_f32_e32 v73, v14, v93
	s_nop 1
	v_cvt_f32_i32_e32 v10, v111
	v_mul_f32_e32 v11, v56, v15
	v_mfma_i32_16x16x64_i8 v[14:17], v[120:123], v[100:103], v[6:9]
	v_mul_f32_e32 v91, v11, v93
	s_nop 1
	v_mul_f32_e32 v6, v57, v10
	v_mul_f32_e32 v94, v93, v6
	v_mfma_i32_16x16x64_i8 v[10:13], v[120:123], v[104:107], v[2:5]
	v_mfma_i32_16x16x64_i8 v[6:9], v[120:123], v[112:115], v[96:99]
	v_mfma_i32_16x16x64_i8 v[2:5], v[120:123], v[124:127], v[84:87]
	s_cbranch_vccz .LBB0_466
	s_and_saveexec_b64 s[8:9], s[6:7]
	s_cbranch_execz .LBB0_465
	v_mov_b32_e32 v67, v137
	v_lshl_add_u64 v[84:85], s[28:29], 0, v[66:67]
	v_lshl_add_u64 v[86:87], v[84:85], 0, v[78:79]
	v_add_co_u32_e32 v86, vcc, 0xffffc000, v86
	s_nop 1
	v_addc_co_u32_e32 v87, vcc, -1, v87, vcc
	global_store_dword v[86:87], v69, off offset:-2048
	v_lshl_add_u64 v[86:87], v[84:85], 0, v[76:77]
	v_add_co_u32_e32 v86, vcc, 0xffffc000, v86
	s_nop 1
	v_addc_co_u32_e32 v87, vcc, -1, v87, vcc
	global_store_dword v[86:87], v73, off offset:-2048
	v_lshl_add_u64 v[86:87], v[84:85], 0, v[74:75]
	v_add_co_u32_e32 v86, vcc, 0xffffc000, v86
	v_lshl_add_u64 v[84:85], v[84:85], 0, v[80:81]
	s_nop 0
	v_addc_co_u32_e32 v87, vcc, -1, v87, vcc
	v_add_co_u32_e32 v84, vcc, 0xffffc000, v84
	global_store_dword v[86:87], v91, off offset:-2048
	s_nop 0
	v_addc_co_u32_e32 v85, vcc, -1, v85, vcc
	global_store_dword v[84:85], v94, off offset:-2048

; template <bool I8 = false, class Epi> ...
;     ...
;       const int col = n0 + wn * 64 + j * 16 + (lane & 15);
;       if (I8) {
;         typedef __attribute__((ext_vector_type(4))) int i32x4;
;         const i32x4 ia = __builtin_bit_cast(i32x4, acc[i][j]);
;         const float cs = cscale[col];
;         epi(row, col, f32x4{(float)ia[0] * rs.x * cs, (float)ia[1] * rs.y * cs, (float)ia[2] * rs.z * cs, (float)ia[3] * rs.w * cs});
;       } else {
;         epi(row, col, acc[i][j]);
;       }
;     }
;   __device__ __forceinline__ void operator()(int row, int col, f32x4 v) const {
;     if (col < 2048) {
;       int ch = col & 1023, half = col >> 10;
;       int b = row / seqlen, l = row - b * seqlen;
;       uint2 pk; pk.x = pack2(v[0], v[1]); pk.y = pack2(v[2], v[3]);
;       *reinterpret_cast<uint2*>(ABt + ((size_t)(b * 1024 + ch) * 4096 + half * 2048 + l)) = pk;
;     } else if (col < 3072) {
; #pragma unroll
;       for (int r = 0; r < 4; ++r) z[(size_t)(row + r) * 1024 + (col - 2048)] = f2bf(v[r]);
;     } else if (col < 4608) {
; #pragma unroll
;       for (int r = 0; r < 4; ++r) xbcraw[(size_t)(row + r) * DXBC + (col - 3072)] = f2bf(v[r]);
;     } else if (col < 4640) {
; #pragma unroll
;       for (int r = 0; r < 4; ++r) dtraw[(size_t)(row + r) * 32 + (col - 4608)] = v[r];
;     }
;   }
.LBB0_468:
	v_or_b32_e32 v67, 16, v92
	v_lshlrev_b32_e32 v72, 2, v67
	v_mov_b32_e32 v69, v225
	v_cvt_f32_i32_e32 v62, v62
	v_cvt_f32_i32_e32 v63, v63
	v_cvt_f32_i32_e32 v64, v64
	v_cvt_f32_i32_e32 v65, v65
	v_mul_f32_e32 v62, v54, v62
	v_mul_f32_e32 v63, v55, v63
	v_mul_f32_e32 v64, v56, v64
	v_mul_f32_e32 v65, v57, v65
	v_cmp_gt_u32_e64 s[6:7], s97, v92
	v_cmp_lt_u32_e64 s[8:9], s89, v92
	v_mul_f32_e32 v91, v62, v69
	v_mul_f32_e32 v90, v63, v69
	v_mul_f32_e32 v63, v64, v69
	v_mul_f32_e32 v62, v65, v69
	s_and_saveexec_b64 s[10:11], s[8:9]
	s_xor_b64 s[10:11], exec, s[10:11]
	s_cbranch_execz .LBB0_472
	v_cmp_gt_u32_e32 vcc, s90, v92
	s_and_saveexec_b64 s[14:15], vcc
	s_cbranch_execz .LBB0_471
	v_mov_b32_e32 v73, v137
	v_lshl_add_u64 v[64:65], s[28:29], 0, v[72:73]
	v_lshl_add_u64 v[94:95], v[64:65], 0, v[78:79]
	v_add_co_u32_e32 v94, vcc, 0xffffc000, v94
	s_nop 1
	v_addc_co_u32_e32 v95, vcc, -1, v95, vcc
	global_store_dword v[94:95], v91, off offset:-2048
	v_lshl_add_u64 v[94:95], v[64:65], 0, v[76:77]
	v_add_co_u32_e32 v94, vcc, 0xffffc000, v94
	s_nop 1
	v_addc_co_u32_e32 v95, vcc, -1, v95, vcc
	global_store_dword v[94:95], v90, off offset:-2048
	v_lshl_add_u64 v[90:91], v[64:65], 0, v[74:75]
	v_add_co_u32_e32 v90, vcc, 0xffffc000, v90
	v_lshl_add_u64 v[64:65], v[64:65], 0, v[80:81]
	s_nop 0
	v_addc_co_u32_e32 v91, vcc, -1, v91, vcc
	v_add_co_u32_e32 v64, vcc, 0xffffc000, v64
	global_store_dword v[90:91], v63, off offset:-2048
	s_nop 0
	v_addc_co_u32_e32 v65, vcc, -1, v65, vcc
	global_store_dword v[64:65], v62, off offset:-2048

; template <bool I8 = false, class Epi> ...
;     ...
;       const int col = n0 + wn * 64 + j * 16 + (lane & 15);
;       if (I8) {
;         typedef __attribute__((ext_vector_type(4))) int i32x4;
;         const i32x4 ia = __builtin_bit_cast(i32x4, acc[i][j]);
;         const float cs = cscale[col];
;         epi(row, col, f32x4{(float)ia[0] * rs.x * cs, (float)ia[1] * rs.y * cs, (float)ia[2] * rs.z * cs, (float)ia[3] * rs.w * cs});
;       } else {
;         epi(row, col, acc[i][j]);
;       }
;     }
;   __device__ __forceinline__ void operator()(int row, int col, f32x4 v) const {
;     if (col < 2048) {
;       int ch = col & 1023, half = col >> 10;
;       int b = row / seqlen, l = row - b * seqlen;
;       uint2 pk; pk.x = pack2(v[0], v[1]); pk.y = pack2(v[2], v[3]);
;       *reinterpret_cast<uint2*>(ABt + ((size_t)(b * 1024 + ch) * 4096 + half * 2048 + l)) = pk;
;     } else if (col < 3072) {
; #pragma unroll
;       for (int r = 0; r < 4; ++r) z[(size_t)(row + r) * 1024 + (col - 2048)] = f2bf(v[r]);
;     } else if (col < 4608) {
; #pragma unroll
;       for (int r = 0; r < 4; ++r) xbcraw[(size_t)(row + r) * DXBC + (col - 3072)] = f2bf(v[r]);
;     } else if (col < 4640) {
; #pragma unroll
;       for (int r = 0; r < 4; ++r) dtraw[(size_t)(row + r) * 32 + (col - 4608)] = v[r];
;     }
;   }
.LBB0_474:
	s_or_b64 exec, exec, s[10:11]
	v_or_b32_e32 v65, 32, v92
	v_lshlrev_b32_e32 v62, 2, v65
	v_mov_b32_e32 v90, v226
	v_cvt_f32_i32_e32 v58, v58
	v_cvt_f32_i32_e32 v59, v59
	v_cvt_f32_i32_e32 v60, v60
	v_cvt_f32_i32_e32 v61, v61
	v_cndmask_b32_e64 v63, 0, 1, s[12:13]
	v_mul_f32_e32 v58, v54, v58
	v_mul_f32_e32 v59, v55, v59
	v_mul_f32_e32 v60, v56, v60
	v_mul_f32_e32 v61, v57, v61
	v_cmp_lt_u32_e64 s[10:11], s93, v92
	v_cmp_ne_u32_e64 s[12:13], 1, v63
	v_mul_f32_e32 v73, v58, v90
	v_mul_f32_e32 v67, v59, v90
	v_mul_f32_e32 v59, v60, v90
	v_mul_f32_e32 v58, v61, v90
	s_and_saveexec_b64 s[14:15], s[10:11]
	s_xor_b64 s[14:15], exec, s[14:15]
	s_cbranch_execz .LBB0_477
	s_and_b64 vcc, exec, s[12:13]
	s_cbranch_vccnz .LBB0_477
	v_mov_b32_e32 v63, v137
	v_lshl_add_u64 v[60:61], s[28:29], 0, v[62:63]
	v_lshl_add_u64 v[94:95], v[60:61], 0, v[78:79]
	v_add_co_u32_e32 v94, vcc, 0xffffc000, v94
	s_nop 1
	v_addc_co_u32_e32 v95, vcc, -1, v95, vcc
	global_store_dword v[94:95], v73, off offset:-2048
	v_lshl_add_u64 v[94:95], v[60:61], 0, v[76:77]
	v_add_co_u32_e32 v94, vcc, 0xffffc000, v94
	s_nop 1
	v_addc_co_u32_e32 v95, vcc, -1, v95, vcc
	global_store_dword v[94:95], v67, off offset:-2048
	v_lshl_add_u64 v[94:95], v[60:61], 0, v[74:75]
	v_add_co_u32_e32 v94, vcc, 0xffffc000, v94
	v_lshl_add_u64 v[60:61], v[60:61], 0, v[80:81]
	s_nop 0
	v_addc_co_u32_e32 v95, vcc, -1, v95, vcc
	v_add_co_u32_e32 v60, vcc, 0xffffc000, v60
	global_store_dword v[94:95], v59, off offset:-2048
	s_nop 0
	v_addc_co_u32_e32 v61, vcc, -1, v61, vcc
	global_store_dword v[60:61], v58, off offset:-2048

; template <bool I8 = false, class Epi> ...
;     ...
;       const int col = n0 + wn * 64 + j * 16 + (lane & 15);
;       if (I8) {
;         typedef __attribute__((ext_vector_type(4))) int i32x4;
;         const i32x4 ia = __builtin_bit_cast(i32x4, acc[i][j]);
;         const float cs = cscale[col];
;         epi(row, col, f32x4{(float)ia[0] * rs.x * cs, (float)ia[1] * rs.y * cs, (float)ia[2] * rs.z * cs, (float)ia[3] * rs.w * cs});
;       } else {
;         epi(row, col, acc[i][j]);
;       }
;     }
;   __device__ __forceinline__ void operator()(int row, int col, f32x4 v) const {
;     if (col < 2048) {
;       int ch = col & 1023, half = col >> 10;
;       int b = row / seqlen, l = row - b * seqlen;
;       uint2 pk; pk.x = pack2(v[0], v[1]); pk.y = pack2(v[2], v[3]);
;       *reinterpret_cast<uint2*>(ABt + ((size_t)(b * 1024 + ch) * 4096 + half * 2048 + l)) = pk;
;     } else if (col < 3072) {
; #pragma unroll
;       for (int r = 0; r < 4; ++r) z[(size_t)(row + r) * 1024 + (col - 2048)] = f2bf(v[r]);
;     } else if (col < 4608) {
; #pragma unroll
;       for (int r = 0; r < 4; ++r) xbcraw[(size_t)(row + r) * DXBC + (col - 3072)] = f2bf(v[r]);
;     } else if (col < 4640) {
; #pragma unroll
;       for (int r = 0; r < 4; ++r) dtraw[(size_t)(row + r) * 32 + (col - 4608)] = v[r];
;     }
;   }
.LBB0_479:
	s_or_b64 exec, exec, s[14:15]
	v_or_b32_e32 v61, 48, v92
	v_lshlrev_b32_e32 v58, 2, v61
	v_mov_b32_e32 v91, v227
	v_cvt_f32_i32_e32 v50, v50
	v_cvt_f32_i32_e32 v51, v51
	v_cvt_f32_i32_e32 v52, v52
	v_cvt_f32_i32_e32 v53, v53
	v_mul_f32_e32 v50, v54, v50
	v_mul_f32_e32 v51, v55, v51
	v_mul_f32_e32 v54, v56, v52
	v_mul_f32_e32 v55, v57, v53
	v_cmp_lt_u32_e64 s[14:15], s96, v92
	v_mul_f32_e32 v53, v50, v91
	v_mul_f32_e32 v52, v51, v91
	v_mul_f32_e32 v51, v54, v91
	v_mul_f32_e32 v50, v55, v91
	s_and_saveexec_b64 s[16:17], s[14:15]
	s_xor_b64 s[16:17], exec, s[16:17]
	s_cbranch_execz .LBB0_483
	s_and_saveexec_b64 s[78:79], s[6:7]
	s_cbranch_execz .LBB0_482
	v_mov_b32_e32 v59, v137
	v_lshl_add_u64 v[54:55], s[28:29], 0, v[58:59]
	v_lshl_add_u64 v[56:57], v[54:55], 0, v[78:79]
	v_add_co_u32_e32 v56, vcc, 0xffffc000, v56
	s_nop 1
	v_addc_co_u32_e32 v57, vcc, -1, v57, vcc
	global_store_dword v[56:57], v53, off offset:-2048
	v_lshl_add_u64 v[56:57], v[54:55], 0, v[76:77]
	v_add_co_u32_e32 v56, vcc, 0xffffc000, v56
	s_nop 1
	v_addc_co_u32_e32 v57, vcc, -1, v57, vcc
	global_store_dword v[56:57], v52, off offset:-2048
	v_lshl_add_u64 v[52:53], v[54:55], 0, v[74:75]
	v_add_co_u32_e32 v52, vcc, 0xffffc000, v52
	s_nop 1
	v_addc_co_u32_e32 v53, vcc, -1, v53, vcc
	global_store_dword v[52:53], v51, off offset:-2048
	v_lshl_add_u64 v[52:53], v[54:55], 0, v[80:81]
	v_add_co_u32_e32 v52, vcc, 0xffffc000, v52
	s_nop 1
	v_addc_co_u32_e32 v53, vcc, -1, v53, vcc
	global_store_dword v[52:53], v50, off offset:-2048

; template <bool I8 = false, class Epi> ...
;     ...
; #pragma unroll
;   for (int i = 0; i < 4; ++i) {
;     const int row = m0 + wm * 64 + i * 16 + (lane >> 4) * 4;
;     float4 rs = float4{1.f, 1.f, 1.f, 1.f};
;     if (I8) rs = *reinterpret_cast<const float4*>(rscale + row);
; #pragma unroll
;     for (int j = 0; j < 4; ++j) {
;       const int col = n0 + wn * 64 + j * 16 + (lane & 15);
;       if (I8) {
;         typedef __attribute__((ext_vector_type(4))) int i32x4;
;         const i32x4 ia = __builtin_bit_cast(i32x4, acc[i][j]);
;         const float cs = cscale[col];
;         epi(row, col, f32x4{(float)ia[0] * rs.x * cs, (float)ia[1] * rs.y * cs, (float)ia[2] * rs.z * cs, (float)ia[3] * rs.w * cs});
;       } else {
;         epi(row, col, acc[i][j]);
;       }
;     }
;   __device__ __forceinline__ void operator()(int row, int col, f32x4 v) const {
;     if (col < 2048) {
;       int ch = col & 1023, half = col >> 10;
;       int b = row / seqlen, l = row - b * seqlen;
;       uint2 pk; pk.x = pack2(v[0], v[1]); pk.y = pack2(v[2], v[3]);
;       *reinterpret_cast<uint2*>(ABt + ((size_t)(b * 1024 + ch) * 4096 + half * 2048 + l)) = pk;
;     } else if (col < 3072) {
; #pragma unroll
;       for (int r = 0; r < 4; ++r) z[(size_t)(row + r) * 1024 + (col - 2048)] = f2bf(v[r]);
;     } else if (col < 4608) {
; #pragma unroll
;       for (int r = 0; r < 4; ++r) xbcraw[(size_t)(row + r) * DXBC + (col - 3072)] = f2bf(v[r]);
;     } else if (col < 4640) {
; #pragma unroll
;       for (int r = 0; r < 4; ++r) dtraw[(size_t)(row + r) * 32 + (col - 4608)] = v[r];
;     }
;   }
.LBB0_485:
	s_or_b64 exec, exec, s[16:17]
	v_mov_b32_e32 v50, v212
	v_mov_b32_e32 v51, v213
	v_mov_b32_e32 v52, v214
	v_mov_b32_e32 v53, v215
	v_cvt_f32_i32_e32 v55, v46
	v_cvt_f32_i32_e32 v59, v47
	v_cvt_f32_i32_e32 v61, v48
	v_cvt_f32_i32_e32 v63, v49
	v_or_b32_e32 v80, 16, v68
	v_or_b32_e32 v76, 17, v68
	v_or_b32_e32 v84, 18, v68
	v_or_b32_e32 v78, 19, v68
	v_cndmask_b32_e64 v46, 0, 1, s[76:77]
	v_ashrrev_i32_e32 v81, 31, v80
	v_ashrrev_i32_e32 v77, 31, v76
	v_ashrrev_i32_e32 v85, 31, v84
	v_ashrrev_i32_e32 v79, 31, v78
	v_cmp_ne_u32_e64 s[16:17], 1, v46
	v_lshlrev_b64 v[74:75], 7, v[80:81]
	v_lshlrev_b64 v[56:57], 7, v[76:77]
	v_lshlrev_b64 v[48:49], 7, v[84:85]
	v_lshlrev_b64 v[46:47], 7, v[78:79]
	s_andn2_b64 vcc, exec, s[76:77]
	s_mov_b64 s[76:77], -1
	v_mul_f32_e32 v55, v50, v55
	v_mul_f32_e32 v59, v51, v59
	v_mul_f32_e32 v65, v52, v61
	v_mul_f32_e32 v67, v53, v63
	v_mul_f32_e32 v63, v93, v55
	v_mul_f32_e32 v61, v93, v59
	v_mul_f32_e32 v59, v93, v65
	v_mul_f32_e32 v55, v93, v67
	s_cbranch_vccnz .LBB0_489
	v_cmp_gt_u32_e32 vcc, s85, v92
	s_and_saveexec_b64 s[76:77], vcc
	s_cbranch_execz .LBB0_488
	v_mov_b32_e32 v67, v137
	v_lshl_add_u64 v[82:83], s[28:29], 0, v[66:67]
	v_lshl_add_u64 v[86:87], v[82:83], 0, v[74:75]
	v_add_co_u32_e32 v86, vcc, 0xffffc000, v86
	s_nop 1
	v_addc_co_u32_e32 v87, vcc, -1, v87, vcc
	global_store_dword v[86:87], v63, off offset:-2048
	v_lshl_add_u64 v[86:87], v[82:83], 0, v[56:57]
	v_add_co_u32_e32 v86, vcc, 0xffffc000, v86
	s_nop 1
	v_addc_co_u32_e32 v87, vcc, -1, v87, vcc
	global_store_dword v[86:87], v61, off offset:-2048
	v_lshl_add_u64 v[86:87], v[82:83], 0, v[48:49]
	v_add_co_u32_e32 v86, vcc, 0xffffc000, v86
	v_lshl_add_u64 v[82:83], v[82:83], 0, v[46:47]
	s_nop 0
	v_addc_co_u32_e32 v87, vcc, -1, v87, vcc
	v_add_co_u32_e32 v82, vcc, 0xffffc000, v82
	global_store_dword v[86:87], v59, off offset:-2048
	s_nop 0
	v_addc_co_u32_e32 v83, vcc, -1, v83, vcc
	global_store_dword v[82:83], v55, off offset:-2048

; template <bool I8 = false, class Epi> ...
;     ...
; #pragma unroll
;   for (int i = 0; i < 4; ++i) {
;     const int row = m0 + wm * 64 + i * 16 + (lane >> 4) * 4;
;     float4 rs = float4{1.f, 1.f, 1.f, 1.f};
;     if (I8) rs = *reinterpret_cast<const float4*>(rscale + row);
; #pragma unroll
;     for (int j = 0; j < 4; ++j) {
;       const int col = n0 + wn * 64 + j * 16 + (lane & 15);
;       if (I8) {
;         typedef __attribute__((ext_vector_type(4))) int i32x4;
;         const i32x4 ia = __builtin_bit_cast(i32x4, acc[i][j]);
;         const float cs = cscale[col];
;         epi(row, col, f32x4{(float)ia[0] * rs.x * cs, (float)ia[1] * rs.y * cs, (float)ia[2] * rs.z * cs, (float)ia[3] * rs.w * cs});
;       } else {
;         epi(row, col, acc[i][j]);
;       }
;     }
;   __device__ __forceinline__ void operator()(int row, int col, f32x4 v) const {
;     if (col < 2048) {
;       int ch = col & 1023, half = col >> 10;
;       int b = row / seqlen, l = row - b * seqlen;
;       uint2 pk; pk.x = pack2(v[0], v[1]); pk.y = pack2(v[2], v[3]);
;       *reinterpret_cast<uint2*>(ABt + ((size_t)(b * 1024 + ch) * 4096 + half * 2048 + l)) = pk;
;     } else if (col < 3072) {
; #pragma unroll
;       for (int r = 0; r < 4; ++r) z[(size_t)(row + r) * 1024 + (col - 2048)] = f2bf(v[r]);
;     } else if (col < 4608) {
; #pragma unroll
;       for (int r = 0; r < 4; ++r) xbcraw[(size_t)(row + r) * DXBC + (col - 3072)] = f2bf(v[r]);
;     } else if (col < 4640) {
; #pragma unroll
;       for (int r = 0; r < 4; ++r) dtraw[(size_t)(row + r) * 32 + (col - 4608)] = v[r];
;     }
;   }
.LBB0_508:
	s_or_b64 exec, exec, s[76:77]
	v_mov_b32_e32 v34, v216
	v_mov_b32_e32 v35, v217
	v_mov_b32_e32 v36, v218
	v_mov_b32_e32 v37, v219
	v_cvt_f32_i32_e32 v48, v30
	v_cvt_f32_i32_e32 v49, v31
	v_cvt_f32_i32_e32 v52, v32
	v_cvt_f32_i32_e32 v53, v33
	v_or_b32_e32 v46, 32, v68
	v_or_b32_e32 v42, 33, v68
	v_or_b32_e32 v44, 35, v68
	v_or_b32_e32 v50, 34, v68
	v_ashrrev_i32_e32 v47, 31, v46
	v_ashrrev_i32_e32 v43, 31, v42
	v_ashrrev_i32_e32 v45, 31, v44
	v_ashrrev_i32_e32 v51, 31, v50
	v_lshlrev_b64 v[40:41], 7, v[46:47]
	v_lshlrev_b64 v[38:39], 7, v[42:43]
	v_lshlrev_b64 v[30:31], 7, v[44:45]
	s_and_b64 vcc, exec, s[16:17]
	v_lshlrev_b64 v[32:33], 7, v[50:51]
	s_mov_b64 s[76:77], -1
	v_mul_f32_e32 v43, v34, v48
	v_mul_f32_e32 v45, v35, v49
	v_mul_f32_e32 v47, v36, v52
	v_mul_f32_e32 v48, v37, v53
	v_mul_f32_e32 v55, v93, v43
	v_mul_f32_e32 v53, v93, v45
	v_mul_f32_e32 v52, v93, v47
	v_mul_f32_e32 v51, v93, v48
	s_cbranch_vccnz .LBB0_512
	v_cmp_gt_u32_e32 vcc, s85, v92
	s_and_saveexec_b64 s[76:77], vcc
	s_cbranch_execz .LBB0_511
	v_mov_b32_e32 v67, v137
	v_lshl_add_u64 v[48:49], s[28:29], 0, v[66:67]
	v_lshl_add_u64 v[56:57], v[48:49], 0, v[40:41]
	v_add_co_u32_e32 v56, vcc, 0xffffc000, v56
	s_nop 1
	v_addc_co_u32_e32 v57, vcc, -1, v57, vcc
	global_store_dword v[56:57], v55, off offset:-2048
	v_lshl_add_u64 v[56:57], v[48:49], 0, v[38:39]
	v_add_co_u32_e32 v56, vcc, 0xffffc000, v56
	s_nop 1
	v_addc_co_u32_e32 v57, vcc, -1, v57, vcc
	global_store_dword v[56:57], v53, off offset:-2048
	v_lshl_add_u64 v[56:57], v[48:49], 0, v[32:33]
	v_add_co_u32_e32 v56, vcc, 0xffffc000, v56
	v_lshl_add_u64 v[48:49], v[48:49], 0, v[30:31]
	s_nop 0
	v_addc_co_u32_e32 v57, vcc, -1, v57, vcc
	v_add_co_u32_e32 v48, vcc, 0xffffc000, v48
	global_store_dword v[56:57], v52, off offset:-2048
	s_nop 0
	v_addc_co_u32_e32 v49, vcc, -1, v49, vcc
	global_store_dword v[48:49], v51, off offset:-2048

; template <bool I8 = false, class Epi> ...
;     ...
; #pragma unroll
;   for (int i = 0; i < 4; ++i) {
;     const int row = m0 + wm * 64 + i * 16 + (lane >> 4) * 4;
;     float4 rs = float4{1.f, 1.f, 1.f, 1.f};
;     if (I8) rs = *reinterpret_cast<const float4*>(rscale + row);
; #pragma unroll
;     for (int j = 0; j < 4; ++j) {
;       const int col = n0 + wn * 64 + j * 16 + (lane & 15);
;       if (I8) {
;         typedef __attribute__((ext_vector_type(4))) int i32x4;
;         const i32x4 ia = __builtin_bit_cast(i32x4, acc[i][j]);
;         const float cs = cscale[col];
;         epi(row, col, f32x4{(float)ia[0] * rs.x * cs, (float)ia[1] * rs.y * cs, (float)ia[2] * rs.z * cs, (float)ia[3] * rs.w * cs});
;       } else {
;         epi(row, col, acc[i][j]);
;       }
;     }
;   __device__ __forceinline__ void operator()(int row, int col, f32x4 v) const {
;     if (col < 2048) {
;       int ch = col & 1023, half = col >> 10;
;       int b = row / seqlen, l = row - b * seqlen;
;       uint2 pk; pk.x = pack2(v[0], v[1]); pk.y = pack2(v[2], v[3]);
;       *reinterpret_cast<uint2*>(ABt + ((size_t)(b * 1024 + ch) * 4096 + half * 2048 + l)) = pk;
;     } else if (col < 3072) {
; #pragma unroll
;       for (int r = 0; r < 4; ++r) z[(size_t)(row + r) * 1024 + (col - 2048)] = f2bf(v[r]);
;     } else if (col < 4608) {
; #pragma unroll
;       for (int r = 0; r < 4; ++r) xbcraw[(size_t)(row + r) * DXBC + (col - 3072)] = f2bf(v[r]);
;     } else if (col < 4640) {
; #pragma unroll
;       for (int r = 0; r < 4; ++r) dtraw[(size_t)(row + r) * 32 + (col - 4608)] = v[r];
;     }
;   }
.LBB0_531:
	s_or_b64 exec, exec, s[76:77]
	v_mov_b32_e32 v18, v220
	v_mov_b32_e32 v19, v221
	v_mov_b32_e32 v20, v222
	v_mov_b32_e32 v21, v223
	v_cvt_f32_i32_e32 v32, v14
	v_cvt_f32_i32_e32 v33, v15
	v_cvt_f32_i32_e32 v36, v16
	v_cvt_f32_i32_e32 v37, v17
	v_or_b32_e32 v30, 48, v68
	v_or_b32_e32 v28, 49, v68
	v_or_b32_e32 v26, 51, v68
	v_or_b32_e32 v34, 50, v68
	v_ashrrev_i32_e32 v31, 31, v30
	v_ashrrev_i32_e32 v29, 31, v28
	v_ashrrev_i32_e32 v27, 31, v26
	v_ashrrev_i32_e32 v35, 31, v34
	v_lshlrev_b64 v[24:25], 7, v[30:31]
	v_lshlrev_b64 v[22:23], 7, v[28:29]
	v_lshlrev_b64 v[14:15], 7, v[26:27]
	s_and_b64 vcc, exec, s[16:17]
	v_lshlrev_b64 v[16:17], 7, v[34:35]
	s_mov_b64 s[16:17], -1
	v_mul_f32_e32 v27, v18, v32
	v_mul_f32_e32 v29, v19, v33
	v_mul_f32_e32 v31, v20, v36
	v_mul_f32_e32 v32, v21, v37
	v_mul_f32_e32 v38, v93, v27
	v_mul_f32_e32 v37, v93, v29
	v_mul_f32_e32 v36, v93, v31
	v_mul_f32_e32 v35, v93, v32
	s_cbranch_vccnz .LBB0_535
	v_cmp_gt_u32_e32 vcc, s85, v92
	s_and_saveexec_b64 s[16:17], vcc
	s_cbranch_execz .LBB0_534
	v_mov_b32_e32 v67, v137
	v_lshl_add_u64 v[32:33], s[28:29], 0, v[66:67]
	v_lshl_add_u64 v[40:41], v[32:33], 0, v[24:25]
	v_add_co_u32_e32 v40, vcc, 0xffffc000, v40
	s_nop 1
	v_addc_co_u32_e32 v41, vcc, -1, v41, vcc
	global_store_dword v[40:41], v38, off offset:-2048
	v_lshl_add_u64 v[40:41], v[32:33], 0, v[22:23]
	v_add_co_u32_e32 v40, vcc, 0xffffc000, v40
	s_nop 1
	v_addc_co_u32_e32 v41, vcc, -1, v41, vcc
	global_store_dword v[40:41], v37, off offset:-2048
	v_lshl_add_u64 v[40:41], v[32:33], 0, v[16:17]
	v_add_co_u32_e32 v40, vcc, 0xffffc000, v40
	v_lshl_add_u64 v[32:33], v[32:33], 0, v[14:15]
	s_nop 0
	v_addc_co_u32_e32 v41, vcc, -1, v41, vcc
	v_add_co_u32_e32 v32, vcc, 0xffffc000, v32
	global_store_dword v[40:41], v36, off offset:-2048
	s_nop 0
	v_addc_co_u32_e32 v33, vcc, -1, v33, vcc
	global_store_dword v[32:33], v35, off offset:-2048
